# P1 both layers: adaLN shift1/scale1 chunks from LDS (static region) instead of per-chunk global loads; stacked on P5 LDS params
# speedup vs baseline: 1.0180x; 1.0068x over previous
; #define GAS __attribute__((address_space(1)))
; #define LAS __attribute__((address_space(3)))
; __device__ __forceinline__ f32x4 bf4(unsigned a, unsigned b) { return (f32x4){bflo(a), bfhi(a), bflo(b), bfhi(b)}; }
; __device__ __forceinline__ void refresh(Frame& F) { int l = (int)__builtin_amdgcn_mbcnt_hi(~0u, __builtin_amdgcn_mbcnt_lo(~0u, 0u)); asm volatile("" : "+v"(l)); F.lane = l; F.tid = F.wave * 64 + l; }
; template <int l>
; __device__ __forceinline__ void layer_phases(Frame& F, const XcdBarrier& bar, const int lo, const int hi) {
;     ...
;         if (IN(pb - 1)) for (int rep = 0; rep < NREP(1); ++rep) {
;             refresh(F);
;             LAS unsigned char* hs = F.lds + RING_OFF;
;             LAS float* part = (LAS float*)(F.lds + RING_OFF);
;             const unsigned char* wff = ws + WS_WF + (size_t)l * 262144;
;             const float* Fx = inptr<const float>(F, I_X); const bf16* Xb = (const bf16*)(ws + WS_X2B);
;             bf16* hbuf = (bf16*)(ws + WS_H); float* flog = (float*)(ws + WS_FLOG);
;             for (int item_ = blockIdx.x; item_ < T / 32; item_ += F.G) {
;                 const int ia_ = affine_item(item_, F.G);
;                 const int item = (l == 1) ? ((F.G == 256) ? ((ia_ & ~63) + 63 - (ia_ & 63)) : (T / 32 - 1 - item_)) : ia_;
;                 const int m0 = item * 32 + 4 * F.wave;
;                 int lq = F.lane; asm volatile("" : "+v"(lq));
;                 const int r32 = lq & 31, hi5 = lq >> 5;
;                 const float* mrow = (const float*)(ws + WS_MOD) + ((size_t)l * 8 + (m0 >> 11)) * 12288;
;                 f32x4 xv[4][8];
; #pragma unroll
;                 for (int rr = 0; rr < 4; ++rr)
; #pragma unroll
;                     for (int j = 0; j < 8; ++j) { const size_t o0 = (size_t)(m0 + rr) * D + 4 * lq + 256 * j;
;                         if (l == 0) xv[rr][j] = __builtin_nontemporal_load((const GAS f32x4*)(Fx + o0)); else { const v2u a = __builtin_nontemporal_load((const GAS v2u*)(Xb + o0)); xv[rr][j] = bf4(a.x, a.y); } }
; #pragma unroll
;                 for (int j = 0; j < 8; ++j) { const int k = 4 * lq + 256 * j;
;                     const f32x4 sh = *(const GAS f32x4*)(mrow + k), sc = *(const GAS f32x4*)(mrow + 2048 + k) + 1.0f;
.LBB0_132:
	s_cmp_gt_i32 s92, 1
	s_cselect_b64 s[0:1], -1, 0
	s_cmp_lt_i32 s93, 2
	s_cselect_b64 s[4:5], -1, 0
	s_or_b64 s[0:1], s[0:1], s[4:5]
	s_and_b64 vcc, exec, s[0:1]
	s_cbranch_vccnz .LBB0_194
	s_add_i32 s0, 0, 0x21400
	v_mov_b32_e32 v129, v216
	v_mov_b32_e32 v0, s0
	ds_read_b64 v[0:1], v0
	v_readlane_b32 s0, v248, 0
	s_mov_b32 s1, 0
	s_cmpk_gt_i32 s2, 0x1ff
	v_add_u32_e32 v128, s0, v129
	s_waitcnt lgkmcnt(0)
	v_readfirstlane_b32 s7, v1
	v_readfirstlane_b32 s6, v0
	s_cbranch_scc1 .LBB0_140
	s_add_u32 s8, s56, 0x35c00000
	s_addc_u32 s9, s57, 0
	s_add_u32 s3, s56, 0x100000
	s_addc_u32 s22, s57, 0
	s_cmpk_eq_i32 s76, 0x100
	s_cselect_b64 s[4:5], -1, 0
	s_lshl_b32 s23, s80, 2
	s_lshl_b32 s0, s80, 14
	s_add_i32 s24, s0, 0
	s_or_b32 s0, s23, 1
	s_mov_b32 s12, 0x2aaaaaab
	s_lshl_b32 s10, s0, 12
	s_and_b32 s27, s0, 13
	s_or_b32 s0, s23, 2
	v_mul_hi_i32 v0, v128, s12
	s_add_i32 s26, s10, 0
	s_lshl_b32 s10, s0, 12
	s_and_b32 s29, s0, 14
	s_or_b32 s0, s23, 3
	v_lshrrev_b32_e32 v1, 31, v0
	v_ashrrev_i32_e32 v0, 1, v0
	s_add_i32 s28, s10, 0
	s_lshl_b32 s10, s0, 12
	s_and_b32 s31, s0, 15
	s_lshl_b32 s0, s80, 4
	v_add_u32_e32 v130, v0, v1
	s_and_b32 s25, s23, 12
	s_add_i32 s30, s10, 0
	s_lshl_b64 s[0:1], s[0:1], 11
	v_mul_lo_u32 v0, v130, 12
	s_add_u32 s0, s56, s0
	v_sub_u32_e32 v0, v128, v0
	s_addc_u32 s1, s57, s1
	v_lshlrev_b32_e32 v1, 7, v130
	v_lshlrev_b32_e32 v2, 2, v0
	s_add_u32 s10, s0, 0x6fa00000
	v_add3_u32 v131, 0, v1, v2
	v_ashrrev_i32_e32 v1, 31, v0
	s_addc_u32 s11, s1, 0
	s_lshl_b32 s0, s80, 12
	v_lshl_add_u64 v[0:1], v[0:1], 2, s[56:57]
	s_mov_b64 s[12:13], 0x600000
	s_add_i32 s35, s0, 0
	s_movk_i32 s0, 0x180
	v_lshl_add_u64 v[96:97], v[0:1], 0, s[12:13]
	v_cndmask_b32_e64 v0, 0, 1, s[4:5]
	s_lshl_b32 s34, s80, 5
	v_cmp_gt_i32_e64 s[0:1], s0, v128
	s_lshl_b32 s36, s2, 6
	s_lshl_b32 s37, s76, 6
	v_cmp_ne_u32_e64 s[4:5], 1, v0
	s_movk_i32 s38, 0x1000
	s_mov_b64 s[12:13], 0x2000
	s_movk_i32 s39, 0x2000
	s_movk_i32 s40, 0x7fff
	s_mov_b32 s41, 0xffff0000
	s_movk_i32 s42, 0x3000
	s_movk_i32 s43, 0x4000
	s_movk_i32 s44, 0x5000
	s_movk_i32 s45, 0x6000
	s_movk_i32 s46, 0x7000
	s_mov_b32 s47, s2
	s_lshl_b32 s98, s80, 10
	v_lshl_add_u32 v253, v216, 4, s98
	s_and_b32 s100, s2, 7
	s_add_u32 s100, s100, 0
	s_mul_i32 s100, s100, 0xc000
	s_add_u32 s100, s100, 0x100000
	s_add_u32 s98, s56, s100
	s_addc_u32 s99, s57, 0
	global_load_dwordx4 v[100:103], v253, s[98:99]
	s_add_u32 s98, s98, 0x2000
	s_addc_u32 s99, s99, 0
	global_load_dwordx4 v[104:107], v253, s[98:99]
	v_add_u32_e32 v253, 0x24000, v253
	s_waitcnt vmcnt(1)
	ds_write_b128 v253, v[100:103]
	s_waitcnt vmcnt(0)
	ds_write_b128 v253, v[104:107] offset:8192
	v_lshlrev_b32_e32 v252, 4, v216
	v_add_u32_e32 v252, 0x24000, v252
	s_waitcnt lgkmcnt(0)
	s_barrier
	s_branch .LBB0_136

; #define GAS __attribute__((address_space(1)))
; #define LAS __attribute__((address_space(3)))
; __device__ __forceinline__ unsigned pk2(float lo, float hi) { return f2bf(lo) | (f2bf(hi) << 16); }
; __device__ __forceinline__ f32x4 bf4(unsigned a, unsigned b) { return (f32x4){bflo(a), bfhi(a), bflo(b), bfhi(b)}; }
; template <int l>
; __device__ __forceinline__ void layer_phases(Frame& F, const XcdBarrier& bar, const int lo, const int hi) {
;     ...
;                 f32x4 xv[4][8];
; #pragma unroll
;                 for (int rr = 0; rr < 4; ++rr)
; #pragma unroll
;                     for (int j = 0; j < 8; ++j) { const size_t o0 = (size_t)(m0 + rr) * D + 4 * lq + 256 * j;
;                         if (l == 0) xv[rr][j] = __builtin_nontemporal_load((const GAS f32x4*)(Fx + o0)); else { const v2u a = __builtin_nontemporal_load((const GAS v2u*)(Xb + o0)); xv[rr][j] = bf4(a.x, a.y); } }
; #pragma unroll
;                 for (int j = 0; j < 8; ++j) { const int k = 4 * lq + 256 * j;
;                     const f32x4 sh = *(const GAS f32x4*)(mrow + k), sc = *(const GAS f32x4*)(mrow + 2048 + k) + 1.0f;
; #pragma unroll
;                     for (int rr = 0; rr < 4; ++rr) { const int rloc = 4 * F.wave + rr; const f32x4 h = xv[rr][j] * sc + sh;
;                         v2u o; o.x = pk2(h.x, h.y); o.y = pk2(h.z, h.w);
;                         *(GAS v2u*)(hbuf + (size_t)(m0 + rr) * D + k) = o;
;                         const int chunk = (lq >> 1) + 32 * j;
;                         *(LAS v2u*)(hs + rloc * 4096 + ((chunk ^ (rloc & 15)) << 4) + (lq & 1) * 8) = o; } }
.LBB0_138:
	s_lshl_b32 s48, s14, 5
	s_add_i32 s14, s48, s23
	s_ashr_i32 s15, s14, 11
	s_or_b32 s16, s14, 1
	s_or_b32 s18, s14, 2
	s_or_b32 s20, s14, 3
	v_mov_b32_e32 v132, v129
	s_mul_hi_i32 s33, s15, 0xc000
	s_mul_i32 s49, s15, 0xc000
	s_ashr_i32 s15, s14, 31
	s_ashr_i32 s17, s16, 31
	s_ashr_i32 s19, s18, 31
	s_ashr_i32 s21, s20, 31
	s_lshl_b64 s[50:51], s[14:15], 13
	v_lshlrev_b32_e32 v12, 2, v132
	s_lshl_b64 s[52:53], s[16:17], 13
	s_lshl_b64 s[54:55], s[18:19], 13
	s_lshl_b64 s[58:59], s[20:21], 13
	v_ashrrev_i32_e32 v13, 31, v12
	s_add_u32 s60, s3, s49
	v_lshlrev_b64 v[0:1], 2, v[12:13]
	s_addc_u32 s61, s22, s33
	v_lshl_add_u64 v[124:125], s[60:61], 0, v[0:1]
	v_lshl_add_u64 v[2:3], s[6:7], 0, v[0:1]
	v_add_co_u32_e32 v98, vcc, s42, v124
	v_lshl_add_u64 v[0:1], v[2:3], 0, s[50:51]
	s_nop 0
	v_addc_co_u32_e32 v99, vcc, 0, v125, vcc
	ds_read_b128 v[28:31], v252 offset:0
	ds_read_b128 v[44:47], v252 offset:8192
	global_load_dwordx4 v[60:63], v[0:1], off nt
	v_lshl_add_u64 v[4:5], v[2:3], 0, s[52:53]
	global_load_dwordx4 v[76:79], v[4:5], off nt
	v_lshl_add_u64 v[6:7], v[2:3], 0, s[54:55]
	global_load_dwordx4 v[92:95], v[6:7], off nt
	v_lshl_add_u64 v[14:15], v[2:3], 0, s[58:59]
	global_load_dwordx4 v[116:119], v[0:1], off offset:1024 nt
	global_load_dwordx4 v[88:91], v[0:1], off offset:2048 nt
	global_load_dwordx4 v[72:75], v[0:1], off offset:3072 nt
	global_load_dwordx4 v[100:103], v[14:15], off nt
	v_add_co_u32_e32 v0, vcc, s38, v0
	global_load_dwordx4 v[120:123], v[4:5], off offset:1024 nt
	global_load_dwordx4 v[84:87], v[4:5], off offset:2048 nt
	global_load_dwordx4 v[68:71], v[4:5], off offset:3072 nt
	v_addc_co_u32_e32 v1, vcc, 0, v1, vcc
	v_add_co_u32_e32 v4, vcc, s38, v4
	global_load_dwordx4 v[134:137], v[6:7], off offset:1024 nt
	global_load_dwordx4 v[80:83], v[6:7], off offset:2048 nt
	global_load_dwordx4 v[64:67], v[6:7], off offset:3072 nt
	v_addc_co_u32_e32 v5, vcc, 0, v5, vcc
	v_add_co_u32_e32 v8, vcc, s38, v6
	global_load_dwordx4 v[138:141], v[14:15], off offset:1024 nt
	s_nop 0
	v_addc_co_u32_e32 v9, vcc, 0, v7, vcc
	v_add_co_u32_e32 v108, vcc, s38, v14
	global_load_dwordx4 v[56:59], v[0:1], off nt
	global_load_dwordx4 v[40:43], v[0:1], off offset:1024 nt
	global_load_dwordx4 v[16:19], v[0:1], off offset:2048 nt
	s_nop 0
	global_load_dwordx4 v[0:3], v[0:1], off offset:3072 nt
	s_nop 0
	global_load_dwordx4 v[52:55], v[4:5], off nt
	global_load_dwordx4 v[36:39], v[4:5], off offset:1024 nt
	global_load_dwordx4 v[20:23], v[4:5], off offset:2048 nt
	s_nop 0
	global_load_dwordx4 v[4:7], v[4:5], off offset:3072 nt
	s_nop 0
	global_load_dwordx4 v[48:51], v[8:9], off nt
	global_load_dwordx4 v[32:35], v[8:9], off offset:1024 nt
	global_load_dwordx4 v[24:27], v[8:9], off offset:2048 nt
	s_nop 0
	global_load_dwordx4 v[8:11], v[8:9], off offset:3072 nt
	v_addc_co_u32_e32 v109, vcc, 0, v15, vcc
	s_lshl_b64 s[14:15], s[14:15], 12
	v_lshl_add_u64 v[126:127], v[124:125], 0, s[12:13]
	s_waitcnt lgkmcnt(0)
	v_pk_add_f32 v[44:45], v[44:45], 1.0 op_sel_hi:[1,0]
	s_waitcnt vmcnt(25)
	v_pk_fma_f32 v[60:61], v[60:61], v[44:45], v[28:29]
	v_pk_add_f32 v[46:47], v[46:47], 1.0 op_sel_hi:[1,0]
	v_bfe_u32 v104, v60, 16, 1
	v_bfe_u32 v105, v61, 16, 1
	v_add3_u32 v60, v60, v104, s40
	v_pk_fma_f32 v[62:63], v[62:63], v[46:47], v[30:31]
	s_waitcnt vmcnt(24)
	v_pk_fma_f32 v[76:77], v[76:77], v[44:45], v[28:29]
	v_add3_u32 v61, v61, v105, s40
	v_lshrrev_b32_e32 v60, 16, v60
	v_bfe_u32 v106, v62, 16, 1
	v_and_or_b32 v104, v61, s41, v60
	v_bfe_u32 v60, v76, 16, 1
	v_bfe_u32 v107, v63, 16, 1
	v_add3_u32 v62, v62, v106, s40
	v_add3_u32 v60, v76, v60, s40
	v_bfe_u32 v61, v77, 16, 1
	v_pk_fma_f32 v[78:79], v[78:79], v[46:47], v[30:31]
	v_add3_u32 v63, v63, v107, s40
	v_lshrrev_b32_e32 v62, 16, v62
	v_lshrrev_b32_e32 v60, 16, v60
	v_add3_u32 v61, v77, v61, s40
	v_and_or_b32 v105, v63, s41, v62
	v_and_or_b32 v106, v61, s41, v60
	v_bfe_u32 v60, v78, 16, 1
	s_waitcnt vmcnt(23)
	v_pk_fma_f32 v[62:63], v[92:93], v[44:45], v[28:29]
	v_add3_u32 v60, v78, v60, s40
	v_bfe_u32 v61, v79, 16, 1
	v_bfe_u32 v76, v62, 16, 1
	v_lshrrev_b32_e32 v60, 16, v60
	v_add3_u32 v61, v79, v61, s40
	v_add3_u32 v62, v62, v76, s40
	v_bfe_u32 v76, v63, 16, 1
	s_waitcnt vmcnt(19)
	v_pk_fma_f32 v[28:29], v[100:101], v[44:45], v[28:29]
	v_and_or_b32 v107, v61, s41, v60
	v_pk_fma_f32 v[60:61], v[94:95], v[46:47], v[30:31]
	v_add3_u32 v63, v63, v76, s40
	global_load_dwordx4 v[92:95], v[14:15], off offset:2048 nt
	global_load_dwordx4 v[76:79], v[14:15], off offset:3072 nt
	v_pk_fma_f32 v[14:15], v[102:103], v[46:47], v[30:31]
	v_bfe_u32 v30, v28, 16, 1
	v_lshrrev_b32_e32 v62, 16, v62
	v_add3_u32 v28, v28, v30, s40
	v_bfe_u32 v30, v29, 16, 1
	v_and_or_b32 v112, v63, s41, v62
	v_bfe_u32 v62, v60, 16, 1
	v_add3_u32 v29, v29, v30, s40
	v_bfe_u32 v30, v14, 16, 1
	v_add3_u32 v60, v60, v62, s40
	v_bfe_u32 v62, v61, 16, 1
	v_add3_u32 v14, v14, v30, s40
	v_bfe_u32 v30, v15, 16, 1
	v_lshl_add_u64 v[100:101], v[12:13], 1, s[8:9]
	v_lshrrev_b32_e32 v12, 16, v28
	v_lshrrev_b32_e32 v60, 16, v60
	v_add3_u32 v61, v61, v62, s40
	v_add3_u32 v15, v15, v30, s40
	v_and_or_b32 v114, v29, s41, v12
	v_lshrrev_b32_e32 v12, 16, v14
	v_and_or_b32 v113, v61, s41, v60
	global_load_dwordx4 v[60:63], v[108:109], off nt
	global_load_dwordx4 v[44:47], v[108:109], off offset:1024 nt
	v_and_or_b32 v115, v15, s41, v12
	global_load_dwordx4 v[28:31], v[108:109], off offset:2048 nt
	global_load_dwordx4 v[12:15], v[108:109], off offset:3072 nt
	v_lshl_add_u64 v[108:109], v[100:101], 0, s[14:15]
	s_lshl_b64 s[14:15], s[16:17], 12
	v_lshl_add_u64 v[110:111], v[100:101], 0, s[14:15]
	s_lshl_b64 s[14:15], s[18:19], 12
	v_lshl_add_u64 v[102:103], v[100:101], 0, s[14:15]
	s_lshl_b64 s[14:15], s[20:21], 12
	v_lshl_add_u64 v[100:101], v[100:101], 0, s[14:15]
	global_store_dwordx2 v[108:109], v[104:105], off
	global_store_dwordx2 v[110:111], v[106:107], off
	global_store_dwordx2 v[102:103], v[112:113], off
	global_store_dwordx2 v[100:101], v[114:115], off
	ds_read_b128 v[142:145], v252 offset:9216
	ds_read_b128 v[146:149], v252 offset:1024
	s_waitcnt vmcnt(4) lgkmcnt(0)
; #define GAS __attribute__((address_space(1)))
; #define LAS __attribute__((address_space(3)))
; __device__ __forceinline__ unsigned pk2(float lo, float hi) { return f2bf(lo) | (f2bf(hi) << 16); }
; template <int l>
; __device__ __forceinline__ void layer_phases(Frame& F, const XcdBarrier& bar, const int lo, const int hi) {
;     ...
; #pragma unroll
;                 for (int j = 0; j < 8; ++j) { const int k = 4 * lq + 256 * j;
;                     const f32x4 sh = *(const GAS f32x4*)(mrow + k), sc = *(const GAS f32x4*)(mrow + 2048 + k) + 1.0f;
; #pragma unroll
;                     for (int rr = 0; rr < 4; ++rr) { const int rloc = 4 * F.wave + rr; const f32x4 h = xv[rr][j] * sc + sh;
;                         v2u o; o.x = pk2(h.x, h.y); o.y = pk2(h.z, h.w);
;                         *(GAS v2u*)(hbuf + (size_t)(m0 + rr) * D + k) = o;
;                         const int chunk = (lq >> 1) + 32 * j;
;                         *(LAS v2u*)(hs + rloc * 4096 + ((chunk ^ (rloc & 15)) << 4) + (lq & 1) * 8) = o; } }
	v_pk_add_f32 v[144:145], v[144:145], 1.0 op_sel_hi:[1,0]
	v_pk_add_f32 v[142:143], v[142:143], 1.0 op_sel_hi:[1,0]
	v_pk_fma_f32 v[118:119], v[118:119], v[144:145], v[148:149]
	v_pk_fma_f32 v[116:117], v[116:117], v[142:143], v[146:147]
	v_pk_fma_f32 v[120:121], v[120:121], v[142:143], v[146:147]
	v_pk_fma_f32 v[134:135], v[134:135], v[142:143], v[146:147]
	v_pk_fma_f32 v[138:139], v[138:139], v[142:143], v[146:147]
	v_bfe_u32 v133, v116, 16, 1
	v_bfe_u32 v143, v118, 16, 1
	v_pk_fma_f32 v[122:123], v[122:123], v[144:145], v[148:149]
	v_pk_fma_f32 v[136:137], v[136:137], v[144:145], v[148:149]
	v_pk_fma_f32 v[140:141], v[140:141], v[144:145], v[148:149]
	v_bfe_u32 v142, v117, 16, 1
	v_bfe_u32 v144, v119, 16, 1
	v_add3_u32 v116, v116, v133, s40
	v_add3_u32 v118, v118, v143, s40
	v_bfe_u32 v145, v120, 16, 1
	v_add3_u32 v117, v117, v142, s40
	v_add3_u32 v119, v119, v144, s40
	v_lshrrev_b32_e32 v116, 16, v116
	v_lshrrev_b32_e32 v118, 16, v118
	v_bfe_u32 v146, v121, 16, 1
	v_add3_u32 v120, v120, v145, s40
	v_and_or_b32 v116, v117, s41, v116
	v_and_or_b32 v117, v119, s41, v118
	v_bfe_u32 v119, v122, 16, 1
	v_add3_u32 v118, v121, v146, s40
	v_add3_u32 v119, v122, v119, s40
	v_bfe_u32 v121, v123, 16, 1
	v_lshrrev_b32_e32 v120, 16, v120
	v_add3_u32 v121, v123, v121, s40
	v_and_or_b32 v118, v118, s41, v120
	v_lshrrev_b32_e32 v119, 16, v119
	v_bfe_u32 v120, v134, 16, 1
	v_and_or_b32 v119, v121, s41, v119
	v_add3_u32 v120, v134, v120, s40
	v_bfe_u32 v121, v135, 16, 1
	v_bfe_u32 v122, v136, 16, 1
	v_add3_u32 v121, v135, v121, s40
	v_add3_u32 v122, v136, v122, s40
	v_bfe_u32 v123, v137, 16, 1
	v_lshrrev_b32_e32 v120, 16, v120
	v_add3_u32 v123, v137, v123, s40
	v_and_or_b32 v120, v121, s41, v120
	v_lshrrev_b32_e32 v121, 16, v122
	v_bfe_u32 v122, v138, 16, 1
	v_and_or_b32 v121, v123, s41, v121
	v_add3_u32 v122, v138, v122, s40
	v_bfe_u32 v123, v139, 16, 1
	v_bfe_u32 v133, v140, 16, 1
	v_add3_u32 v123, v139, v123, s40
	v_add3_u32 v133, v140, v133, s40
	v_bfe_u32 v134, v141, 16, 1
	v_lshrrev_b32_e32 v122, 16, v122
	v_add3_u32 v134, v141, v134, s40
	v_and_or_b32 v122, v123, s41, v122
	v_lshrrev_b32_e32 v123, 16, v133
	v_and_or_b32 v123, v134, s41, v123
	global_store_dwordx2 v[108:109], v[116:117], off offset:512
	global_store_dwordx2 v[110:111], v[118:119], off offset:512
	global_store_dwordx2 v[102:103], v[120:121], off offset:512
	global_store_dwordx2 v[100:101], v[122:123], off offset:512
	ds_read_b128 v[134:137], v252 offset:10240
	ds_read_b128 v[138:141], v252 offset:2048
	s_waitcnt lgkmcnt(0)
	v_pk_add_f32 v[136:137], v[136:137], 1.0 op_sel_hi:[1,0]
	v_pk_add_f32 v[134:135], v[134:135], 1.0 op_sel_hi:[1,0]
	v_pk_fma_f32 v[90:91], v[90:91], v[136:137], v[140:141]
	v_pk_fma_f32 v[86:87], v[86:87], v[136:137], v[140:141]
	v_pk_fma_f32 v[88:89], v[88:89], v[134:135], v[138:139]
	v_pk_fma_f32 v[84:85], v[84:85], v[134:135], v[138:139]
	v_pk_fma_f32 v[82:83], v[82:83], v[136:137], v[140:141]
	v_pk_fma_f32 v[80:81], v[80:81], v[134:135], v[138:139]
	v_pk_fma_f32 v[92:93], v[92:93], v[134:135], v[138:139]
	v_bfe_u32 v135, v90, 16, 1
	v_bfe_u32 v139, v86, 16, 1
	v_pk_fma_f32 v[94:95], v[94:95], v[136:137], v[140:141]
	v_bfe_u32 v133, v88, 16, 1
	v_bfe_u32 v134, v89, 16, 1
	v_bfe_u32 v136, v91, 16, 1
	v_bfe_u32 v140, v87, 16, 1
	v_bfe_u32 v142, v81, 16, 1
	v_bfe_u32 v143, v82, 16, 1
	v_bfe_u32 v144, v83, 16, 1
	v_add3_u32 v90, v90, v135, s40
	v_add3_u32 v86, v86, v139, s40
	v_add3_u32 v88, v88, v133, s40
	v_add3_u32 v89, v89, v134, s40
	v_add3_u32 v91, v91, v136, s40
	v_add3_u32 v87, v87, v140, s40
	v_add3_u32 v133, v81, v142, s40
	v_add3_u32 v81, v82, v143, s40
	v_add3_u32 v134, v83, v144, s40
	v_lshrrev_b32_e32 v83, 16, v90
	v_lshrrev_b32_e32 v86, 16, v86
	v_lshrrev_b32_e32 v90, 16, v81
	v_and_or_b32 v81, v91, s41, v83
	v_and_or_b32 v83, v87, s41, v86
	v_bfe_u32 v86, v92, 16, 1
	v_bfe_u32 v137, v84, 16, 1
	v_bfe_u32 v141, v80, 16, 1
	v_add3_u32 v86, v92, v86, s40
	v_bfe_u32 v87, v93, 16, 1
	v_bfe_u32 v138, v85, 16, 1
	v_add3_u32 v84, v84, v137, s40
	v_add3_u32 v80, v80, v141, s40
	v_lshrrev_b32_e32 v86, 16, v86
	v_add3_u32 v87, v93, v87, s40
	v_add3_u32 v85, v85, v138, s40
	v_lshrrev_b32_e32 v82, 16, v88
	v_lshrrev_b32_e32 v84, 16, v84
	v_lshrrev_b32_e32 v88, 16, v80
	v_and_or_b32 v86, v87, s41, v86
	v_bfe_u32 v87, v94, 16, 1
	v_and_or_b32 v80, v89, s41, v82
	v_and_or_b32 v82, v85, s41, v84
	v_and_or_b32 v84, v133, s41, v88
	v_add3_u32 v87, v94, v87, s40
	v_bfe_u32 v88, v95, 16, 1
	v_lshrrev_b32_e32 v87, 16, v87
	v_add3_u32 v88, v95, v88, s40
	v_and_or_b32 v87, v88, s41, v87
	v_and_or_b32 v85, v134, s41, v90
	global_store_dwordx2 v[108:109], v[80:81], off offset:1024
	global_store_dwordx2 v[110:111], v[82:83], off offset:1024
	global_store_dwordx2 v[102:103], v[84:85], off offset:1024
	global_store_dwordx2 v[100:101], v[86:87], off offset:1024
	ds_read_b128 v[88:91], v252 offset:11264
	ds_read_b128 v[92:95], v252 offset:3072
	s_waitcnt lgkmcnt(0)
; #define GAS __attribute__((address_space(1)))
; #define LAS __attribute__((address_space(3)))
; __device__ __forceinline__ unsigned pk2(float lo, float hi) { return f2bf(lo) | (f2bf(hi) << 16); }
; template <int l>
; __device__ __forceinline__ void layer_phases(Frame& F, const XcdBarrier& bar, const int lo, const int hi) {
;     ...
; #pragma unroll
;                 for (int j = 0; j < 8; ++j) { const int k = 4 * lq + 256 * j;
;                     const f32x4 sh = *(const GAS f32x4*)(mrow + k), sc = *(const GAS f32x4*)(mrow + 2048 + k) + 1.0f;
; #pragma unroll
;                     for (int rr = 0; rr < 4; ++rr) { const int rloc = 4 * F.wave + rr; const f32x4 h = xv[rr][j] * sc + sh;
;                         v2u o; o.x = pk2(h.x, h.y); o.y = pk2(h.z, h.w);
;                         *(GAS v2u*)(hbuf + (size_t)(m0 + rr) * D + k) = o;
;                         const int chunk = (lq >> 1) + 32 * j;
;                         *(LAS v2u*)(hs + rloc * 4096 + ((chunk ^ (rloc & 15)) << 4) + (lq & 1) * 8) = o; } }
	v_pk_add_f32 v[90:91], v[90:91], 1.0 op_sel_hi:[1,0]
	v_pk_add_f32 v[88:89], v[88:89], 1.0 op_sel_hi:[1,0]
	v_pk_fma_f32 v[74:75], v[74:75], v[90:91], v[94:95]
	v_pk_fma_f32 v[72:73], v[72:73], v[88:89], v[92:93]
	v_pk_fma_f32 v[70:71], v[70:71], v[90:91], v[94:95]
	v_pk_fma_f32 v[68:69], v[68:69], v[88:89], v[92:93]
	v_pk_fma_f32 v[66:67], v[66:67], v[90:91], v[94:95]
	v_pk_fma_f32 v[64:65], v[64:65], v[88:89], v[92:93]
	v_pk_fma_f32 v[78:79], v[78:79], v[90:91], v[94:95]
	v_pk_fma_f32 v[76:77], v[76:77], v[88:89], v[92:93]
	v_bfe_u32 v88, v72, 16, 1
	v_bfe_u32 v90, v74, 16, 1
	v_bfe_u32 v89, v73, 16, 1
	v_bfe_u32 v91, v75, 16, 1
	v_bfe_u32 v92, v68, 16, 1
	v_bfe_u32 v94, v70, 16, 1
	v_bfe_u32 v126, v64, 16, 1
	v_bfe_u32 v127, v65, 16, 1
	v_bfe_u32 v133, v66, 16, 1
	v_bfe_u32 v134, v67, 16, 1
	v_bfe_u32 v135, v76, 16, 1
	v_bfe_u32 v137, v78, 16, 1
	v_add3_u32 v72, v72, v88, s40
	v_add3_u32 v74, v74, v90, s40
	v_bfe_u32 v93, v69, 16, 1
	v_bfe_u32 v95, v71, 16, 1
	v_bfe_u32 v136, v77, 16, 1
	v_bfe_u32 v138, v79, 16, 1
	v_add3_u32 v73, v73, v89, s40
	v_add3_u32 v75, v75, v91, s40
	v_add3_u32 v68, v68, v92, s40
	v_add3_u32 v70, v70, v94, s40
	v_add3_u32 v64, v64, v126, s40
	v_add3_u32 v88, v65, v127, s40
	v_add3_u32 v65, v66, v133, s40
	v_add3_u32 v89, v67, v134, s40
	v_add3_u32 v66, v76, v135, s40
	v_add3_u32 v67, v78, v137, s40
	v_lshrrev_b32_e32 v72, 16, v72
	v_lshrrev_b32_e32 v74, 16, v74
	v_add3_u32 v69, v69, v93, s40
	v_add3_u32 v71, v71, v95, s40
	v_add3_u32 v76, v77, v136, s40
	v_add3_u32 v77, v79, v138, s40
	v_lshrrev_b32_e32 v68, 16, v68
	v_lshrrev_b32_e32 v70, 16, v70
	v_lshrrev_b32_e32 v78, 16, v64
	v_lshrrev_b32_e32 v79, 16, v65
	v_lshrrev_b32_e32 v90, 16, v66
	v_lshrrev_b32_e32 v91, 16, v67
	v_and_or_b32 v64, v73, s41, v72
	v_and_or_b32 v65, v75, s41, v74
	v_and_or_b32 v66, v69, s41, v68
	v_and_or_b32 v67, v71, s41, v70
	v_and_or_b32 v68, v88, s41, v78
	v_and_or_b32 v69, v89, s41, v79
	v_and_or_b32 v70, v76, s41, v90
	v_and_or_b32 v71, v77, s41, v91
	global_store_dwordx2 v[108:109], v[64:65], off offset:1536
	global_store_dwordx2 v[110:111], v[66:67], off offset:1536
	global_store_dwordx2 v[102:103], v[68:69], off offset:1536
	global_store_dwordx2 v[100:101], v[70:71], off offset:1536
	v_add_co_u32_e32 v72, vcc, s38, v124
	ds_read_b128 v[74:77], v252 offset:12288
	s_nop 0
	v_addc_co_u32_e32 v73, vcc, 0, v125, vcc
	ds_read_b128 v[88:91], v252 offset:4096
	s_waitcnt lgkmcnt(0)
	v_pk_add_f32 v[76:77], v[76:77], 1.0 op_sel_hi:[1,0]
	v_pk_add_f32 v[74:75], v[74:75], 1.0 op_sel_hi:[1,0]
	v_pk_fma_f32 v[58:59], v[58:59], v[76:77], v[90:91]
	v_pk_fma_f32 v[56:57], v[56:57], v[74:75], v[88:89]
	v_pk_fma_f32 v[54:55], v[54:55], v[76:77], v[90:91]
	v_pk_fma_f32 v[52:53], v[52:53], v[74:75], v[88:89]
	v_pk_fma_f32 v[50:51], v[50:51], v[76:77], v[90:91]
	v_pk_fma_f32 v[48:49], v[48:49], v[74:75], v[88:89]
	v_pk_fma_f32 v[62:63], v[62:63], v[76:77], v[90:91]
	v_pk_fma_f32 v[60:61], v[60:61], v[74:75], v[88:89]
	v_bfe_u32 v74, v56, 16, 1
	v_bfe_u32 v76, v58, 16, 1
	v_bfe_u32 v75, v57, 16, 1
	v_bfe_u32 v77, v59, 16, 1
	v_bfe_u32 v78, v52, 16, 1
	v_bfe_u32 v88, v54, 16, 1
	v_bfe_u32 v90, v48, 16, 1
	v_bfe_u32 v91, v49, 16, 1
	v_bfe_u32 v92, v50, 16, 1
	v_bfe_u32 v93, v51, 16, 1
	v_bfe_u32 v94, v60, 16, 1
	v_bfe_u32 v124, v62, 16, 1
	v_add3_u32 v56, v56, v74, s40
	v_add3_u32 v58, v58, v76, s40
	v_bfe_u32 v79, v53, 16, 1
	v_bfe_u32 v89, v55, 16, 1
	v_bfe_u32 v95, v61, 16, 1
	v_bfe_u32 v125, v63, 16, 1
	v_add3_u32 v57, v57, v75, s40
	v_add3_u32 v59, v59, v77, s40
	v_add3_u32 v52, v52, v78, s40
	v_add3_u32 v54, v54, v88, s40
	v_add3_u32 v48, v48, v90, s40
	v_add3_u32 v74, v49, v91, s40
	v_add3_u32 v49, v50, v92, s40
	v_add3_u32 v75, v51, v93, s40
	v_add3_u32 v50, v60, v94, s40
	v_add3_u32 v51, v62, v124, s40
	v_lshrrev_b32_e32 v56, 16, v56
	v_lshrrev_b32_e32 v58, 16, v58
	v_add3_u32 v53, v53, v79, s40
	v_add3_u32 v55, v55, v89, s40
	v_add3_u32 v60, v61, v95, s40
	v_add3_u32 v61, v63, v125, s40
	v_lshrrev_b32_e32 v52, 16, v52
	v_lshrrev_b32_e32 v54, 16, v54
	v_lshrrev_b32_e32 v62, 16, v48
	v_lshrrev_b32_e32 v63, 16, v49
	v_lshrrev_b32_e32 v76, 16, v50
	v_lshrrev_b32_e32 v77, 16, v51
	v_and_or_b32 v48, v57, s41, v56
	v_and_or_b32 v49, v59, s41, v58
	v_and_or_b32 v50, v53, s41, v52
	v_and_or_b32 v51, v55, s41, v54
	v_and_or_b32 v52, v74, s41, v62
	v_and_or_b32 v53, v75, s41, v63
	v_and_or_b32 v54, v60, s41, v76
	v_and_or_b32 v55, v61, s41, v77
	global_store_dwordx2 v[108:109], v[48:49], off offset:2048
	global_store_dwordx2 v[110:111], v[50:51], off offset:2048
	global_store_dwordx2 v[102:103], v[52:53], off offset:2048
	global_store_dwordx2 v[100:101], v[54:55], off offset:2048
	ds_read_b128 v[56:59], v252 offset:13312
	ds_read_b128 v[60:63], v252 offset:5120
	s_waitcnt lgkmcnt(0)
; #define GAS __attribute__((address_space(1)))
; #define LAS __attribute__((address_space(3)))
; __device__ __forceinline__ unsigned pk2(float lo, float hi) { return f2bf(lo) | (f2bf(hi) << 16); }
; template <int l>
; __device__ __forceinline__ void layer_phases(Frame& F, const XcdBarrier& bar, const int lo, const int hi) {
;     ...
; #pragma unroll
;                 for (int j = 0; j < 8; ++j) { const int k = 4 * lq + 256 * j;
;                     const f32x4 sh = *(const GAS f32x4*)(mrow + k), sc = *(const GAS f32x4*)(mrow + 2048 + k) + 1.0f;
; #pragma unroll
;                     for (int rr = 0; rr < 4; ++rr) { const int rloc = 4 * F.wave + rr; const f32x4 h = xv[rr][j] * sc + sh;
;                         v2u o; o.x = pk2(h.x, h.y); o.y = pk2(h.z, h.w);
;                         *(GAS v2u*)(hbuf + (size_t)(m0 + rr) * D + k) = o;
;                         const int chunk = (lq >> 1) + 32 * j;
;                         *(LAS v2u*)(hs + rloc * 4096 + ((chunk ^ (rloc & 15)) << 4) + (lq & 1) * 8) = o; } }
;     ...
;                     const bf16x8 af = *(const LAS bf16x8*)(hs + r32 * 4096 + (((2 * ks + hi5) ^ (r32 & 15)) << 4));
	v_pk_add_f32 v[58:59], v[58:59], 1.0 op_sel_hi:[1,0]
	v_pk_add_f32 v[56:57], v[56:57], 1.0 op_sel_hi:[1,0]
	v_pk_fma_f32 v[42:43], v[42:43], v[58:59], v[62:63]
	v_pk_fma_f32 v[40:41], v[40:41], v[56:57], v[60:61]
	v_pk_fma_f32 v[38:39], v[38:39], v[58:59], v[62:63]
	v_pk_fma_f32 v[36:37], v[36:37], v[56:57], v[60:61]
	v_pk_fma_f32 v[34:35], v[34:35], v[58:59], v[62:63]
	v_pk_fma_f32 v[32:33], v[32:33], v[56:57], v[60:61]
	v_pk_fma_f32 v[46:47], v[46:47], v[58:59], v[62:63]
	v_pk_fma_f32 v[44:45], v[44:45], v[56:57], v[60:61]
	v_bfe_u32 v56, v40, 16, 1
	v_bfe_u32 v58, v42, 16, 1
	v_bfe_u32 v57, v41, 16, 1
	v_bfe_u32 v59, v43, 16, 1
	v_bfe_u32 v60, v36, 16, 1
	v_bfe_u32 v62, v38, 16, 1
	v_bfe_u32 v74, v32, 16, 1
	v_bfe_u32 v75, v33, 16, 1
	v_bfe_u32 v76, v34, 16, 1
	v_bfe_u32 v77, v35, 16, 1
	v_bfe_u32 v78, v44, 16, 1
	v_bfe_u32 v88, v46, 16, 1
	v_add3_u32 v40, v40, v56, s40
	v_add3_u32 v42, v42, v58, s40
	v_bfe_u32 v61, v37, 16, 1
	v_bfe_u32 v63, v39, 16, 1
	v_bfe_u32 v79, v45, 16, 1
	v_bfe_u32 v89, v47, 16, 1
	v_add3_u32 v41, v41, v57, s40
	v_add3_u32 v43, v43, v59, s40
	v_add3_u32 v36, v36, v60, s40
	v_add3_u32 v38, v38, v62, s40
	v_add3_u32 v32, v32, v74, s40
	v_add3_u32 v56, v33, v75, s40
	v_add3_u32 v33, v34, v76, s40
	v_add3_u32 v57, v35, v77, s40
	v_add3_u32 v34, v44, v78, s40
	v_add3_u32 v35, v46, v88, s40
	v_lshrrev_b32_e32 v40, 16, v40
	v_lshrrev_b32_e32 v42, 16, v42
	v_add3_u32 v37, v37, v61, s40
	v_add3_u32 v39, v39, v63, s40
	v_add3_u32 v44, v45, v79, s40
	v_add3_u32 v45, v47, v89, s40
	v_lshrrev_b32_e32 v36, 16, v36
	v_lshrrev_b32_e32 v38, 16, v38
	v_lshrrev_b32_e32 v46, 16, v32
	v_lshrrev_b32_e32 v47, 16, v33
	v_lshrrev_b32_e32 v58, 16, v34
	v_lshrrev_b32_e32 v59, 16, v35
	v_and_or_b32 v32, v41, s41, v40
	v_and_or_b32 v33, v43, s41, v42
	v_and_or_b32 v34, v37, s41, v36
	v_and_or_b32 v35, v39, s41, v38
	v_and_or_b32 v36, v56, s41, v46
	v_and_or_b32 v37, v57, s41, v47
	v_and_or_b32 v38, v44, s41, v58
	v_and_or_b32 v39, v45, s41, v59
	global_store_dwordx2 v[108:109], v[32:33], off offset:2560
	global_store_dwordx2 v[110:111], v[34:35], off offset:2560
	global_store_dwordx2 v[102:103], v[36:37], off offset:2560
	global_store_dwordx2 v[100:101], v[38:39], off offset:2560
	ds_read_b128 v[40:43], v252 offset:14336
	ds_read_b128 v[44:47], v252 offset:6144
	v_lshrrev_b32_e32 v56, 1, v132
	v_lshlrev_b32_e32 v57, 3, v132
	v_xor_b32_e32 v58, s25, v56
	v_add_u32_e32 v62, 32, v56
	v_add_u32_e32 v63, 64, v56
	v_add_u32_e32 v74, 0x60, v56
	v_add_u32_e32 v75, 0x80, v56
	v_add_u32_e32 v76, 0xa0, v56
	v_add_u32_e32 v77, 0xc0, v56
	v_and_b32_e32 v57, 8, v57
	v_xor_b32_e32 v59, s27, v56
	v_xor_b32_e32 v60, s29, v56
	v_xor_b32_e32 v61, s31, v56
	v_lshlrev_b32_e32 v58, 4, v58
	v_xor_b32_e32 v78, s25, v62
	v_xor_b32_e32 v79, s27, v62
	v_xor_b32_e32 v88, s29, v62
	v_xor_b32_e32 v62, s31, v62
	v_xor_b32_e32 v89, s25, v63
	v_xor_b32_e32 v90, s27, v63
	v_xor_b32_e32 v91, s29, v63
	v_xor_b32_e32 v63, s31, v63
	v_xor_b32_e32 v92, s25, v74
	v_xor_b32_e32 v93, s27, v74
	v_xor_b32_e32 v94, s29, v74
	v_xor_b32_e32 v74, s31, v74
	v_xor_b32_e32 v95, s25, v75
	v_xor_b32_e32 v124, s27, v75
	v_xor_b32_e32 v125, s29, v75
	v_xor_b32_e32 v75, s31, v75
	v_xor_b32_e32 v126, s25, v76
	v_xor_b32_e32 v127, s27, v76
	v_xor_b32_e32 v133, s29, v76
	v_xor_b32_e32 v76, s31, v76
	v_xor_b32_e32 v134, s25, v77
	v_xor_b32_e32 v135, s27, v77
	v_xor_b32_e32 v136, s29, v77
	v_xor_b32_e32 v77, s31, v77
	v_lshlrev_b32_e32 v59, 4, v59
	v_lshlrev_b32_e32 v60, 4, v60
	v_lshlrev_b32_e32 v61, 4, v61
	v_add3_u32 v58, s24, v58, v57
	v_lshlrev_b32_e32 v75, 4, v75
	v_lshlrev_b32_e32 v76, 4, v76
	v_lshlrev_b32_e32 v77, 4, v77
	v_add_u32_e32 v56, 0xe0, v56
	v_add3_u32 v59, s26, v59, v57
	v_add3_u32 v60, s28, v60, v57
	v_add3_u32 v61, s30, v61, v57
	v_add3_u32 v75, s30, v75, v57
	v_add3_u32 v76, s30, v76, v57
	v_add3_u32 v77, s30, v77, v57
	v_xor_b32_e32 v137, s25, v56
	v_xor_b32_e32 v138, s27, v56
	s_waitcnt lgkmcnt(0)
	v_pk_add_f32 v[42:43], v[42:43], 1.0 op_sel_hi:[1,0]
	v_pk_add_f32 v[40:41], v[40:41], 1.0 op_sel_hi:[1,0]
	v_pk_fma_f32 v[18:19], v[18:19], v[42:43], v[46:47]
	v_pk_fma_f32 v[16:17], v[16:17], v[40:41], v[44:45]
	v_pk_fma_f32 v[22:23], v[22:23], v[42:43], v[46:47]
	v_pk_fma_f32 v[20:21], v[20:21], v[40:41], v[44:45]
	v_pk_fma_f32 v[26:27], v[26:27], v[42:43], v[46:47]
	v_pk_fma_f32 v[24:25], v[24:25], v[40:41], v[44:45]
	v_pk_fma_f32 v[30:31], v[30:31], v[42:43], v[46:47]
	v_pk_fma_f32 v[28:29], v[28:29], v[40:41], v[44:45]
	v_bfe_u32 v40, v16, 16, 1
	v_bfe_u32 v42, v18, 16, 1
	v_bfe_u32 v41, v17, 16, 1
	v_bfe_u32 v43, v19, 16, 1
	v_bfe_u32 v44, v20, 16, 1
	v_bfe_u32 v46, v22, 16, 1
	v_bfe_u32 v139, v24, 16, 1
	v_bfe_u32 v140, v25, 16, 1
	v_bfe_u32 v141, v26, 16, 1
	v_bfe_u32 v142, v27, 16, 1
	v_bfe_u32 v143, v28, 16, 1
	v_bfe_u32 v145, v30, 16, 1
	v_add3_u32 v16, v16, v40, s40
	v_add3_u32 v18, v18, v42, s40
	v_bfe_u32 v45, v21, 16, 1
	v_bfe_u32 v47, v23, 16, 1
	v_bfe_u32 v144, v29, 16, 1
	v_bfe_u32 v146, v31, 16, 1
	v_add3_u32 v17, v17, v41, s40
	v_add3_u32 v19, v19, v43, s40
	v_add3_u32 v20, v20, v44, s40
	v_add3_u32 v22, v22, v46, s40
	v_add3_u32 v24, v24, v139, s40
	v_add3_u32 v40, v25, v140, s40
	v_add3_u32 v25, v26, v141, s40
	v_add3_u32 v41, v27, v142, s40
	v_add3_u32 v26, v28, v143, s40
	v_add3_u32 v27, v30, v145, s40
	v_lshrrev_b32_e32 v16, 16, v16
	v_lshrrev_b32_e32 v18, 16, v18
	v_add3_u32 v21, v21, v45, s40
	v_add3_u32 v23, v23, v47, s40
	v_add3_u32 v42, v29, v144, s40
	v_add3_u32 v31, v31, v146, s40
	v_lshrrev_b32_e32 v20, 16, v20
	v_lshrrev_b32_e32 v22, 16, v22
	v_lshrrev_b32_e32 v28, 16, v24
	v_lshrrev_b32_e32 v29, 16, v25
	v_lshrrev_b32_e32 v30, 16, v26
; #define GAS __attribute__((address_space(1)))
; #define LAS __attribute__((address_space(3)))
; __device__ __forceinline__ unsigned pk2(float lo, float hi) { return f2bf(lo) | (f2bf(hi) << 16); }
; template <int l>
; __device__ __forceinline__ void layer_phases(Frame& F, const XcdBarrier& bar, const int lo, const int hi) {
;     ...
; #pragma unroll
;                 for (int j = 0; j < 8; ++j) { const int k = 4 * lq + 256 * j;
;                     const f32x4 sh = *(const GAS f32x4*)(mrow + k), sc = *(const GAS f32x4*)(mrow + 2048 + k) + 1.0f;
; #pragma unroll
;                     for (int rr = 0; rr < 4; ++rr) { const int rloc = 4 * F.wave + rr; const f32x4 h = xv[rr][j] * sc + sh;
;                         v2u o; o.x = pk2(h.x, h.y); o.y = pk2(h.z, h.w);
;                         *(GAS v2u*)(hbuf + (size_t)(m0 + rr) * D + k) = o;
;                         const int chunk = (lq >> 1) + 32 * j;
;                         *(LAS v2u*)(hs + rloc * 4096 + ((chunk ^ (rloc & 15)) << 4) + (lq & 1) * 8) = o; } }
;                 asm volatile("" ::: "memory");
;                 bf16x8 bw[16][2];
;                 { const unsigned char* wb = wff + (size_t)(16 * F.wave) * 2048 + lq * 16;
; #pragma unroll
;                   for (int q = 0; q < 16; ++q) { bw[q][0] = *(const GAS bf16x8*)(wb + q * 2048); bw[q][1] = *(const GAS bf16x8*)(wb + q * 2048 + 1024); } }
	v_lshrrev_b32_e32 v43, 16, v27
	v_and_or_b32 v24, v17, s41, v16
	v_and_or_b32 v25, v19, s41, v18
	v_and_or_b32 v26, v21, s41, v20
	v_and_or_b32 v27, v23, s41, v22
	v_and_or_b32 v28, v40, s41, v28
	v_and_or_b32 v29, v41, s41, v29
	v_and_or_b32 v30, v42, s41, v30
	v_and_or_b32 v31, v31, s41, v43
	global_store_dwordx2 v[108:109], v[24:25], off offset:3072
	global_store_dwordx2 v[110:111], v[26:27], off offset:3072
	global_store_dwordx2 v[102:103], v[28:29], off offset:3072
	global_store_dwordx2 v[100:101], v[30:31], off offset:3072
	ds_read_b128 v[16:19], v252 offset:7168
	ds_read_b128 v[20:23], v252 offset:15360
	v_lshlrev_b32_e32 v40, 4, v78
	v_lshlrev_b32_e32 v41, 4, v79
	v_lshlrev_b32_e32 v42, 4, v88
	v_lshlrev_b32_e32 v43, 4, v62
	v_lshlrev_b32_e32 v44, 4, v89
	v_lshlrev_b32_e32 v45, 4, v90
	v_lshlrev_b32_e32 v46, 4, v91
	v_lshlrev_b32_e32 v47, 4, v63
	v_lshlrev_b32_e32 v62, 4, v92
	v_lshlrev_b32_e32 v63, 4, v93
	v_lshlrev_b32_e32 v72, 4, v94
	v_lshlrev_b32_e32 v73, 4, v74
	v_lshlrev_b32_e32 v74, 4, v95
	v_lshlrev_b32_e32 v78, 4, v124
	v_lshlrev_b32_e32 v79, 4, v125
	v_lshlrev_b32_e32 v88, 4, v126
	v_lshlrev_b32_e32 v89, 4, v127
	v_lshlrev_b32_e32 v90, 4, v133
	v_lshlrev_b32_e32 v91, 4, v134
	v_lshlrev_b32_e32 v92, 4, v135
	v_lshlrev_b32_e32 v93, 4, v136
	v_add3_u32 v40, s24, v40, v57
	v_add3_u32 v41, s26, v41, v57
	v_add3_u32 v42, s28, v42, v57
	v_add3_u32 v43, s30, v43, v57
	v_add3_u32 v44, s24, v44, v57
	v_add3_u32 v45, s26, v45, v57
	v_add3_u32 v46, s28, v46, v57
	v_add3_u32 v47, s30, v47, v57
	v_add3_u32 v62, s24, v62, v57
	v_add3_u32 v63, s26, v63, v57
	v_add3_u32 v72, s28, v72, v57
	v_add3_u32 v73, s30, v73, v57
	v_add3_u32 v74, s24, v74, v57
	v_add3_u32 v78, s26, v78, v57
	v_add3_u32 v79, s28, v79, v57
	v_add3_u32 v88, s24, v88, v57
	v_add3_u32 v89, s26, v89, v57
	v_add3_u32 v90, s28, v90, v57
	v_add3_u32 v91, s24, v91, v57
	v_add3_u32 v92, s26, v92, v57
	v_add3_u32 v93, s28, v93, v57
	ds_write_b64 v58, v[104:105]
	ds_write_b64 v59, v[106:107]
	ds_write_b64 v60, v[112:113]
	ds_write_b64 v61, v[114:115]
	ds_write_b64 v40, v[116:117]
	ds_write_b64 v41, v[118:119]
	ds_write_b64 v42, v[120:121]
	ds_write_b64 v43, v[122:123]
	ds_write_b64 v44, v[80:81]
	ds_write_b64 v45, v[82:83]
	ds_write_b64 v46, v[84:85]
	ds_write_b64 v47, v[86:87]
	ds_write_b64 v62, v[64:65]
	ds_write_b64 v63, v[66:67]
	ds_write_b64 v72, v[68:69]
	ds_write_b64 v73, v[70:71]
	ds_write_b64 v74, v[48:49]
	ds_write_b64 v78, v[50:51]
	ds_write_b64 v79, v[52:53]
	ds_write_b64 v75, v[54:55]
	ds_write_b64 v88, v[32:33]
	ds_write_b64 v89, v[34:35]
	ds_write_b64 v90, v[36:37]
	ds_write_b64 v76, v[38:39]
	ds_write_b64 v91, v[24:25]
	ds_write_b64 v92, v[26:27]
	ds_write_b64 v93, v[28:29]
	ds_write_b64 v77, v[30:31]
	v_lshlrev_b32_e32 v94, 4, v137
	v_lshlrev_b32_e32 v95, 4, v138
	v_add3_u32 v94, s24, v94, v57
	v_ashrrev_i32_e32 v127, 5, v132
	v_and_b32_e32 v126, 31, v132
	v_add_u32_e32 v158, s34, v127
	v_lshl_add_u32 v133, v126, 12, 0
	s_waitcnt lgkmcnt(0)
	v_pk_add_f32 v[22:23], v[22:23], 1.0 op_sel_hi:[1,0]
	v_pk_add_f32 v[20:21], v[20:21], 1.0 op_sel_hi:[1,0]
	v_pk_fma_f32 v[2:3], v[2:3], v[22:23], v[18:19]
	v_pk_fma_f32 v[0:1], v[0:1], v[20:21], v[16:17]
	v_pk_fma_f32 v[6:7], v[6:7], v[22:23], v[18:19]
	v_pk_fma_f32 v[4:5], v[4:5], v[20:21], v[16:17]
	v_bfe_u32 v24, v0, 16, 1
	v_bfe_u32 v26, v2, 16, 1
	v_bfe_u32 v25, v1, 16, 1
	v_bfe_u32 v27, v3, 16, 1
	v_bfe_u32 v28, v4, 16, 1
	v_bfe_u32 v30, v6, 16, 1
	v_add3_u32 v0, v0, v24, s40
	v_add3_u32 v2, v2, v26, s40
	v_bfe_u32 v29, v5, 16, 1
	v_bfe_u32 v31, v7, 16, 1
	v_add3_u32 v1, v1, v25, s40
	v_add3_u32 v3, v3, v27, s40
	v_add3_u32 v4, v4, v28, s40
	v_add3_u32 v6, v6, v30, s40
	v_lshrrev_b32_e32 v0, 16, v0
	v_lshrrev_b32_e32 v2, 16, v2
	v_add3_u32 v5, v5, v29, s40
	v_add3_u32 v7, v7, v31, s40
	v_lshrrev_b32_e32 v4, 16, v4
	v_lshrrev_b32_e32 v6, 16, v6
	v_and_or_b32 v0, v1, s41, v0
	v_and_or_b32 v1, v3, s41, v2
	v_and_or_b32 v2, v5, s41, v4
	v_and_or_b32 v3, v7, s41, v6
	global_store_dwordx2 v[108:109], v[0:1], off offset:3584
	ds_write_b64 v94, v[0:1]
	v_add3_u32 v0, s26, v95, v57
	global_store_dwordx2 v[110:111], v[2:3], off offset:3584
	ds_write_b64 v0, v[2:3]
	v_pk_fma_f32 v[2:3], v[8:9], v[20:21], v[16:17]
	v_pk_fma_f32 v[0:1], v[10:11], v[22:23], v[18:19]
	v_bfe_u32 v4, v2, 16, 1
	v_add3_u32 v2, v2, v4, s40
	v_bfe_u32 v4, v3, 16, 1
	v_lshrrev_b32_e32 v2, 16, v2
	v_add3_u32 v3, v3, v4, s40
	v_and_or_b32 v2, v3, s41, v2
	v_bfe_u32 v3, v0, 16, 1
	v_add3_u32 v0, v0, v3, s40
	v_bfe_u32 v3, v1, 16, 1
	v_lshrrev_b32_e32 v0, 16, v0
	v_add3_u32 v1, v1, v3, s40
	v_and_or_b32 v3, v1, s41, v0
	v_xor_b32_e32 v0, s29, v56
	v_lshlrev_b32_e32 v0, 4, v0
	v_add3_u32 v0, s28, v0, v57
	global_store_dwordx2 v[102:103], v[2:3], off offset:3584
	ds_write_b64 v0, v[2:3]
	v_pk_fma_f32 v[2:3], v[12:13], v[20:21], v[16:17]
	v_pk_fma_f32 v[0:1], v[14:15], v[22:23], v[18:19]
	v_bfe_u32 v4, v2, 16, 1
	v_add3_u32 v2, v2, v4, s40
	v_bfe_u32 v4, v3, 16, 1
	v_lshrrev_b32_e32 v2, 16, v2
	v_add3_u32 v3, v3, v4, s40
	v_and_or_b32 v2, v3, s41, v2
	v_bfe_u32 v3, v0, 16, 1
	v_add3_u32 v0, v0, v3, s40
	v_bfe_u32 v3, v1, 16, 1
	v_lshrrev_b32_e32 v0, 16, v0
	v_add3_u32 v1, v1, v3, s40
	v_and_or_b32 v3, v1, s41, v0
	v_xor_b32_e32 v0, s31, v56
	v_lshlrev_b32_e32 v0, 4, v0
	v_add3_u32 v0, s30, v0, v57
	ds_write_b64 v0, v[2:3]
	v_lshlrev_b32_e32 v0, 4, v132
	global_store_dwordx2 v[100:101], v[2:3], off offset:3584
	v_ashrrev_i32_e32 v1, 31, v0
	v_lshl_add_u64 v[4:5], s[10:11], 0, v[0:1]
	global_load_dwordx4 v[0:3], v[4:5], off
	global_load_dwordx4 v[16:19], v[4:5], off offset:1024
	global_load_dwordx4 v[20:23], v[4:5], off offset:2048
; #define GAS __attribute__((address_space(1)))
; template <int l>
; __device__ __forceinline__ void layer_phases(Frame& F, const XcdBarrier& bar, const int lo, const int hi) {
;     ...
;                 { const unsigned char* wb = wff + (size_t)(16 * F.wave) * 2048 + lq * 16;
; #pragma unroll
;                   for (int q = 0; q < 16; ++q) { bw[q][0] = *(const GAS bf16x8*)(wb + q * 2048); bw[q][1] = *(const GAS bf16x8*)(wb + q * 2048 + 1024); } }
;                 __syncthreads();
	global_load_dwordx4 v[24:27], v[4:5], off offset:3072
	v_add_co_u32_e32 v6, vcc, s38, v4
	s_nop 1
	v_addc_co_u32_e32 v7, vcc, 0, v5, vcc
	v_add_co_u32_e32 v8, vcc, s39, v4
	s_nop 1
	v_addc_co_u32_e32 v9, vcc, 0, v5, vcc
	global_load_dwordx4 v[28:31], v[8:9], off offset:-4096
	global_load_dwordx4 v[32:35], v[6:7], off offset:1024
	global_load_dwordx4 v[36:39], v[6:7], off offset:2048
	global_load_dwordx4 v[40:43], v[8:9], off
	global_load_dwordx4 v[44:47], v[8:9], off offset:1024
	global_load_dwordx4 v[48:51], v[8:9], off offset:2048
	global_load_dwordx4 v[52:55], v[8:9], off offset:3072
	v_add_co_u32_e32 v8, vcc, s42, v4
	s_nop 1
	v_addc_co_u32_e32 v9, vcc, 0, v5, vcc
	v_add_co_u32_e32 v10, vcc, s43, v4
	s_nop 1
	v_addc_co_u32_e32 v11, vcc, 0, v5, vcc
	global_load_dwordx4 v[56:59], v[6:7], off offset:3072
	global_load_dwordx4 v[60:63], v[8:9], off offset:1024
	global_load_dwordx4 v[64:67], v[8:9], off offset:2048
	global_load_dwordx4 v[68:71], v[8:9], off offset:3072
	global_load_dwordx4 v[72:75], v[10:11], off offset:-4096
	global_load_dwordx4 v[76:79], v[10:11], off
	global_load_dwordx4 v[80:83], v[10:11], off offset:1024
	global_load_dwordx4 v[84:87], v[10:11], off offset:2048
	v_add_co_u32_e32 v6, vcc, s44, v4
	s_nop 1
	v_addc_co_u32_e32 v7, vcc, 0, v5, vcc
	v_add_co_u32_e32 v8, vcc, s45, v4
	s_nop 1
	v_addc_co_u32_e32 v9, vcc, 0, v5, vcc
	v_add_co_u32_e32 v4, vcc, s46, v4
	global_load_dwordx4 v[88:91], v[10:11], off offset:3072
	global_load_dwordx4 v[92:95], v[8:9], off offset:-4096
	global_load_dwordx4 v[98:101], v[6:7], off offset:1024
	global_load_dwordx4 v[102:105], v[6:7], off offset:2048
	global_load_dwordx4 v[106:109], v[8:9], off
	global_load_dwordx4 v[110:113], v[8:9], off offset:1024
	global_load_dwordx4 v[114:117], v[8:9], off offset:2048
	global_load_dwordx4 v[118:121], v[8:9], off offset:3072
	v_addc_co_u32_e32 v5, vcc, 0, v5, vcc
	global_load_dwordx4 v[122:125], v[6:7], off offset:3072
	global_load_dwordx4 v[134:137], v[4:5], off
	global_load_dwordx4 v[138:141], v[4:5], off offset:1024
	global_load_dwordx4 v[142:145], v[4:5], off offset:2048
	global_load_dwordx4 v[146:149], v[4:5], off offset:3072
	v_bitop3_b32 v4, v158, v132, 15 bitop3:0x78
	v_lshl_add_u32 v4, v4, 4, v133
	s_waitcnt lgkmcnt(0)
	s_barrier
; #define LAS __attribute__((address_space(3)))
; __device__ __forceinline__ int crow(int r, int hi) { return (r & 3) + 8 * (r >> 2) + 4 * hi; }
; template <int l>
; __device__ __forceinline__ void layer_phases(Frame& F, const XcdBarrier& bar, const int lo, const int hi) {
;     ...
;                 att::f32x16 acc0 = att::f32x16{};
; #pragma unroll
;                 for (int q = 0; q < 16; ++q) { const int ks = 16 * F.wave + q;
;                     const bf16x8 af = *(const LAS bf16x8*)(hs + r32 * 4096 + (((2 * ks + hi5) ^ (r32 & 15)) << 4));
;                     acc0 = __builtin_amdgcn_mfma_f32_32x32x16_bf16(af, bw[q][0], acc0, 0, 0, 0); acc0 = __builtin_amdgcn_mfma_f32_32x32x16_bf16(af, bw[q][1], acc0, 0, 0, 0); }
;                 __syncthreads();
; #pragma unroll
;                 for (int r = 0; r < 16; ++r) part[(F.wave * 32 + att::crow(r, hi5)) * 32 + r32] = acc0[r];
;                 __syncthreads();
;                 if (F.tid < 32 * NFOX) { const int row = F.tid / NFOX, j = F.tid % NFOX; float sacc = 0.f;
; #pragma unroll
;                     for (int w = 0; w < 8; ++w) sacc += part[(w * 32 + row) * 32 + j];
;                     flog[(size_t)(item * 32 + row) * 16 + j] = sacc; }
	ds_read_b128 v[150:153], v4
	v_add_u32_e32 v4, 2, v158
	v_bitop3_b32 v4, v4, v132, 15 bitop3:0x78
	v_lshl_add_u32 v4, v4, 4, v133
	ds_read_b128 v[154:157], v4
	s_waitcnt vmcnt(31) lgkmcnt(1)
	v_mfma_f32_32x32x16_bf16 v[0:15], v[150:153], v[0:3], 0
	s_waitcnt vmcnt(30)
	v_mfma_f32_32x32x16_bf16 v[0:15], v[150:153], v[16:19], v[0:15]
	v_add_u32_e32 v16, 4, v158
	v_bitop3_b32 v16, v16, v132, 15 bitop3:0x78
	v_lshl_add_u32 v16, v16, 4, v133
	ds_read_b128 v[16:19], v16
	s_waitcnt vmcnt(29) lgkmcnt(1)
	v_mfma_f32_32x32x16_bf16 v[0:15], v[154:157], v[20:23], v[0:15]
	v_add_u32_e32 v20, 6, v158
	v_bitop3_b32 v20, v20, v132, 15 bitop3:0x78
	v_lshl_add_u32 v20, v20, 4, v133
	ds_read_b128 v[20:23], v20
	s_waitcnt vmcnt(28)
	v_mfma_f32_32x32x16_bf16 v[0:15], v[154:157], v[24:27], v[0:15]
	s_waitcnt vmcnt(27) lgkmcnt(1)
	v_mfma_f32_32x32x16_bf16 v[0:15], v[16:19], v[28:31], v[0:15]
	s_waitcnt vmcnt(26)
	v_mfma_f32_32x32x16_bf16 v[0:15], v[16:19], v[32:35], v[0:15]
	v_add_u32_e32 v16, 8, v158
	v_bitop3_b32 v16, v16, v132, 15 bitop3:0x78
	v_lshl_add_u32 v16, v16, 4, v133
	ds_read_b128 v[16:19], v16
	s_waitcnt vmcnt(25) lgkmcnt(1)
	v_mfma_f32_32x32x16_bf16 v[0:15], v[20:23], v[36:39], v[0:15]
	s_waitcnt vmcnt(20)
	v_mfma_f32_32x32x16_bf16 v[0:15], v[20:23], v[56:59], v[0:15]
	v_add_u32_e32 v20, 10, v158
	v_bitop3_b32 v20, v20, v132, 15 bitop3:0x78
	v_lshl_add_u32 v20, v20, 4, v133
	ds_read_b128 v[20:23], v20
	s_waitcnt lgkmcnt(1)
	v_mfma_f32_32x32x16_bf16 v[0:15], v[16:19], v[40:43], v[0:15]
	v_mfma_f32_32x32x16_bf16 v[0:15], v[16:19], v[44:47], v[0:15]
	v_add_u32_e32 v16, 12, v158
	v_bitop3_b32 v16, v16, v132, 15 bitop3:0x78
	v_lshl_add_u32 v16, v16, 4, v133
	ds_read_b128 v[16:19], v16
	s_waitcnt lgkmcnt(1)
	v_mfma_f32_32x32x16_bf16 v[0:15], v[20:23], v[48:51], v[0:15]
	v_mfma_f32_32x32x16_bf16 v[0:15], v[20:23], v[52:55], v[0:15]
	v_add_u32_e32 v20, 14, v158
	v_bitop3_b32 v20, v20, v132, 15 bitop3:0x78
	v_lshl_add_u32 v20, v20, 4, v133
	ds_read_b128 v[20:23], v20
	s_waitcnt vmcnt(16) lgkmcnt(1)
	v_mfma_f32_32x32x16_bf16 v[0:15], v[16:19], v[72:75], v[0:15]
	v_mfma_f32_32x32x16_bf16 v[0:15], v[16:19], v[60:63], v[0:15]
	v_add_u32_e32 v16, 16, v158
	v_bitop3_b32 v16, v16, v132, 15 bitop3:0x78
	v_lshl_add_u32 v16, v16, 4, v133
	ds_read_b128 v[16:19], v16
	s_waitcnt lgkmcnt(1)
	v_mfma_f32_32x32x16_bf16 v[0:15], v[20:23], v[64:67], v[0:15]
	v_mfma_f32_32x32x16_bf16 v[0:15], v[20:23], v[68:71], v[0:15]
	v_add_u32_e32 v20, 18, v158
	v_bitop3_b32 v20, v20, v132, 15 bitop3:0x78
	v_lshl_add_u32 v20, v20, 4, v133
	ds_read_b128 v[20:23], v20
	s_waitcnt vmcnt(15) lgkmcnt(1)
	v_mfma_f32_32x32x16_bf16 v[0:15], v[16:19], v[76:79], v[0:15]
	s_waitcnt vmcnt(14)
	v_mfma_f32_32x32x16_bf16 v[0:15], v[16:19], v[80:83], v[0:15]
	v_add_u32_e32 v16, 20, v158
	v_bitop3_b32 v16, v16, v132, 15 bitop3:0x78
	v_lshl_add_u32 v16, v16, 4, v133
	ds_read_b128 v[16:19], v16
	s_waitcnt vmcnt(13) lgkmcnt(1)
	v_mfma_f32_32x32x16_bf16 v[0:15], v[20:23], v[84:87], v[0:15]
	s_waitcnt vmcnt(12)
	v_mfma_f32_32x32x16_bf16 v[0:15], v[20:23], v[88:91], v[0:15]
	v_add_u32_e32 v20, 22, v158
	v_bitop3_b32 v20, v20, v132, 15 bitop3:0x78
	v_lshl_add_u32 v20, v20, 4, v133
	ds_read_b128 v[20:23], v20
	s_waitcnt vmcnt(11) lgkmcnt(1)
	v_mfma_f32_32x32x16_bf16 v[0:15], v[16:19], v[92:95], v[0:15]
	s_waitcnt vmcnt(10)
	v_mfma_f32_32x32x16_bf16 v[0:15], v[16:19], v[98:101], v[0:15]
	v_add_u32_e32 v16, 24, v158
	v_bitop3_b32 v16, v16, v132, 15 bitop3:0x78
	v_lshl_add_u32 v16, v16, 4, v133
	ds_read_b128 v[16:19], v16
	s_waitcnt vmcnt(9) lgkmcnt(1)
	v_mfma_f32_32x32x16_bf16 v[0:15], v[20:23], v[102:105], v[0:15]
	s_waitcnt vmcnt(4)
	v_mfma_f32_32x32x16_bf16 v[0:15], v[20:23], v[122:125], v[0:15]
	v_add_u32_e32 v20, 26, v158
	v_bitop3_b32 v20, v20, v132, 15 bitop3:0x78
	v_lshl_add_u32 v20, v20, 4, v133
	ds_read_b128 v[20:23], v20
	s_waitcnt lgkmcnt(1)
	v_mfma_f32_32x32x16_bf16 v[0:15], v[16:19], v[106:109], v[0:15]
	v_mfma_f32_32x32x16_bf16 v[0:15], v[16:19], v[110:113], v[0:15]
	v_add_u32_e32 v16, 28, v158
	v_bitop3_b32 v16, v16, v132, 15 bitop3:0x78
	v_lshl_add_u32 v16, v16, 4, v133
	ds_read_b128 v[16:19], v16
	s_waitcnt lgkmcnt(1)
	v_mfma_f32_32x32x16_bf16 v[0:15], v[20:23], v[114:117], v[0:15]
	v_mfma_f32_32x32x16_bf16 v[0:15], v[20:23], v[118:121], v[0:15]
	v_add_u32_e32 v20, 30, v158
	v_bitop3_b32 v20, v20, v132, 15 bitop3:0x78
	v_lshl_add_u32 v20, v20, 4, v133
	ds_read_b128 v[20:23], v20
	s_waitcnt lgkmcnt(0)
	s_barrier
	s_waitcnt vmcnt(3)
	v_mfma_f32_32x32x16_bf16 v[0:15], v[16:19], v[134:137], v[0:15]
	s_waitcnt vmcnt(2)
	v_mfma_f32_32x32x16_bf16 v[0:15], v[16:19], v[138:141], v[0:15]
	v_lshlrev_b32_e32 v16, 9, v127
	v_lshlrev_b32_e32 v17, 2, v126
	v_add3_u32 v16, s35, v16, v17
	v_add_u32_e32 v17, 0x400, v16
	v_add_u32_e32 v18, 0x800, v16
	v_add_u32_e32 v19, 0xc00, v16
	s_waitcnt vmcnt(1)
	v_mfma_f32_32x32x16_bf16 v[0:15], v[20:23], v[142:145], v[0:15]
	s_waitcnt vmcnt(0)
	v_mfma_f32_32x32x16_bf16 v[0:15], v[20:23], v[146:149], v[0:15]
	s_nop 11
	ds_write2_b32 v16, v0, v1 offset1:32
	ds_write2_b32 v16, v2, v3 offset0:64 offset1:96
	ds_write2_b32 v17, v4, v5 offset1:32
	ds_write2_b32 v17, v6, v7 offset0:64 offset1:96
	ds_write2_b32 v18, v8, v9 offset1:32
	ds_write2_b32 v18, v10, v11 offset0:64 offset1:96
	ds_write2_b32 v19, v12, v13 offset1:32
	ds_write2_b32 v19, v14, v15 offset0:64 offset1:96
	s_waitcnt lgkmcnt(0)
	s_barrier
	s_and_saveexec_b64 s[14:15], s[0:1]
	s_cbranch_execz .LBB0_135
	ds_read2st64_b32 v[0:1], v131 offset1:16
	ds_read2st64_b32 v[2:3], v131 offset0:32 offset1:48
	ds_read2st64_b32 v[4:5], v131 offset0:64 offset1:80
	ds_read2st64_b32 v[6:7], v131 offset0:96 offset1:112
	v_add_u32_e32 v8, s48, v130
	s_waitcnt lgkmcnt(3)
	v_add_f32_e32 v0, 0, v0
	v_add_f32_e32 v0, v0, v1
	s_waitcnt lgkmcnt(2)
	v_add_f32_e32 v0, v0, v2
	v_add_f32_e32 v0, v0, v3
	s_waitcnt lgkmcnt(1)
	v_add_f32_e32 v0, v0, v4
	v_add_f32_e32 v0, v0, v5
	s_waitcnt lgkmcnt(0)
	v_add_f32_e32 v0, v0, v6
	v_ashrrev_i32_e32 v9, 31, v8
	v_add_f32_e32 v2, v0, v7
	v_lshlrev_b64 v[0:1], 6, v[8:9]
	v_lshl_add_u64 v[0:1], v[96:97], 0, v[0:1]
	global_store_dword v[0:1], v2, off
	s_branch .LBB0_135

; #define GAS __attribute__((address_space(1)))
; #define LAS __attribute__((address_space(3)))
; __device__ __forceinline__ f32x4 bf4(unsigned a, unsigned b) { return (f32x4){bflo(a), bfhi(a), bflo(b), bfhi(b)}; }
; __device__ __forceinline__ void refresh(Frame& F) { int l = (int)__builtin_amdgcn_mbcnt_hi(~0u, __builtin_amdgcn_mbcnt_lo(~0u, 0u)); asm volatile("" : "+v"(l)); F.lane = l; F.tid = F.wave * 64 + l; }
; template <int l>
; __device__ __forceinline__ void layer_phases(Frame& F, const XcdBarrier& bar, const int lo, const int hi) {
;     ...
;         if (IN(pb - 1)) for (int rep = 0; rep < NREP(1); ++rep) {
;             refresh(F);
;             LAS unsigned char* hs = F.lds + RING_OFF;
;             LAS float* part = (LAS float*)(F.lds + RING_OFF);
;             const unsigned char* wff = ws + WS_WF + (size_t)l * 262144;
;             const float* Fx = inptr<const float>(F, I_X); const bf16* Xb = (const bf16*)(ws + WS_X2B);
;             bf16* hbuf = (bf16*)(ws + WS_H); float* flog = (float*)(ws + WS_FLOG);
;             for (int item_ = blockIdx.x; item_ < T / 32; item_ += F.G) {
;                 const int ia_ = affine_item(item_, F.G);
;                 const int item = (l == 1) ? ((F.G == 256) ? ((ia_ & ~63) + 63 - (ia_ & 63)) : (T / 32 - 1 - item_)) : ia_;
;                 const int m0 = item * 32 + 4 * F.wave;
;                 int lq = F.lane; asm volatile("" : "+v"(lq));
;                 const int r32 = lq & 31, hi5 = lq >> 5;
;                 const float* mrow = (const float*)(ws + WS_MOD) + ((size_t)l * 8 + (m0 >> 11)) * 12288;
;                 f32x4 xv[4][8];
; #pragma unroll
;                 for (int rr = 0; rr < 4; ++rr)
; #pragma unroll
;                     for (int j = 0; j < 8; ++j) { const size_t o0 = (size_t)(m0 + rr) * D + 4 * lq + 256 * j;
;                         if (l == 0) xv[rr][j] = __builtin_nontemporal_load((const GAS f32x4*)(Fx + o0)); else { const v2u a = __builtin_nontemporal_load((const GAS v2u*)(Xb + o0)); xv[rr][j] = bf4(a.x, a.y); } }
; #pragma unroll
;                 for (int j = 0; j < 8; ++j) { const int k = 4 * lq + 256 * j;
;                     const f32x4 sh = *(const GAS f32x4*)(mrow + k), sc = *(const GAS f32x4*)(mrow + 2048 + k) + 1.0f;
.LBB0_1042:
	s_cmp_gt_i32 s92, 9
	s_cselect_b64 s[0:1], -1, 0
	s_cmp_lt_i32 s93, 10
	s_cselect_b64 s[4:5], -1, 0
	s_or_b64 s[0:1], s[0:1], s[4:5]
	s_and_b64 vcc, exec, s[0:1]
	s_cbranch_vccnz .LBB0_1104
	s_waitcnt vmcnt(0)
	v_mov_b32_e32 v79, v216
	v_readlane_b32 s0, v248, 0
	s_cmpk_gt_i32 s2, 0x1ff
	s_nop 0
	v_add_u32_e32 v78, s0, v79
	s_cbranch_scc1 .LBB0_1050
	s_add_u32 s6, s56, 0x3dc00000
	s_addc_u32 s7, s57, 0
	s_add_u32 s8, s56, 0x35c00000
	s_addc_u32 s9, s57, 0
	s_add_u32 s3, s56, 0x100000
	s_addc_u32 s24, s57, 0
	s_cmpk_eq_i32 s76, 0x100
	s_cselect_b64 s[10:11], -1, 0
	s_lshl_b32 s25, s80, 2
	s_lshl_b32 s0, s80, 14
	s_add_i32 s26, s0, 0
	s_or_b32 s0, s25, 1
	s_lshl_b32 s4, s0, 12
	s_and_b32 s29, s0, 13
	s_or_b32 s0, s25, 2
	s_add_i32 s28, s4, 0
	s_lshl_b32 s4, s0, 12
	s_and_b32 s31, s0, 14
	s_or_b32 s0, s25, 3
	s_add_i32 s30, s4, 0
	s_lshl_b32 s4, s0, 12
	s_add_i32 s34, s4, 0
	s_mov_b32 s4, 0x2aaaaaab
	v_mul_hi_i32 v0, v78, s4
	v_lshrrev_b32_e32 v1, 31, v0
	v_ashrrev_i32_e32 v0, 1, v0
	s_mov_b32 s1, 0
	s_and_b32 s35, s0, 15
	s_lshl_b32 s0, s80, 4
	v_add_u32_e32 v80, v0, v1
	s_and_b32 s27, s25, 12
	s_lshl_b64 s[0:1], s[0:1], 11
	v_mul_lo_u32 v0, v80, 12
	s_add_u32 s0, s56, s0
	v_sub_u32_e32 v0, v78, v0
	s_addc_u32 s1, s57, s1
	v_lshlrev_b32_e32 v1, 7, v80
	v_lshlrev_b32_e32 v2, 2, v0
	s_add_u32 s12, s0, 0x6fa40000
	v_add3_u32 v81, 0, v1, v2
	v_ashrrev_i32_e32 v1, 31, v0
	s_addc_u32 s13, s1, 0
	s_lshl_b32 s0, s80, 12
	v_lshl_add_u64 v[0:1], v[0:1], 2, s[56:57]
	s_mov_b64 s[4:5], 0x600000
	s_add_i32 s37, s0, 0
	s_movk_i32 s0, 0x180
	v_lshl_add_u64 v[16:17], v[0:1], 0, s[4:5]
	v_cndmask_b32_e64 v0, 0, 1, s[10:11]
	s_lshl_b32 s36, s80, 5
	v_cmp_gt_i32_e64 s[0:1], s0, v78
	s_lshl_b32 s38, s2, 6
	s_lshl_b32 s39, s76, 6
	s_sub_i32 s40, 0x1ff, s2
	v_cmp_ne_u32_e64 s[4:5], 1, v0
	s_mov_b32 s41, 0xffff0000
	s_mov_b64 s[14:15], 0x2000
	s_movk_i32 s42, 0x2000
	s_movk_i32 s43, 0x7fff
	s_movk_i32 s44, 0x1000
	s_movk_i32 s45, 0x3000
	s_movk_i32 s46, 0x4000
	s_movk_i32 s47, 0x5000
	s_movk_i32 s48, 0x6000
	s_movk_i32 s49, 0x7000
	s_mov_b32 s50, s2
	s_lshl_b32 s98, s80, 10
	v_lshl_add_u32 v253, v216, 4, s98
	s_and_b32 s100, s2, 7
	s_add_u32 s100, s100, 8
	s_mul_i32 s100, s100, 0xc000
	s_add_u32 s100, s100, 0x100000
	s_add_u32 s98, s56, s100
	s_addc_u32 s99, s57, 0
	global_load_dwordx4 v[100:103], v253, s[98:99]
	s_add_u32 s98, s98, 0x2000
	s_addc_u32 s99, s99, 0
	global_load_dwordx4 v[104:107], v253, s[98:99]
	v_add_u32_e32 v253, 0x24000, v253
	s_waitcnt vmcnt(1)
	ds_write_b128 v253, v[100:103]
	s_waitcnt vmcnt(0)
	ds_write_b128 v253, v[104:107] offset:8192
	v_lshlrev_b32_e32 v252, 4, v216
	v_add_u32_e32 v252, 0x24000, v252
	s_waitcnt lgkmcnt(0)
	s_barrier
	s_branch .LBB0_1046

; #define GAS __attribute__((address_space(1)))
; #define LAS __attribute__((address_space(3)))
; __device__ __forceinline__ unsigned pk2(float lo, float hi) { return f2bf(lo) | (f2bf(hi) << 16); }
; __device__ __forceinline__ f32x4 bf4(unsigned a, unsigned b) { return (f32x4){bflo(a), bfhi(a), bflo(b), bfhi(b)}; }
; template <int l>
; __device__ __forceinline__ void layer_phases(Frame& F, const XcdBarrier& bar, const int lo, const int hi) {
;     ...
;                 f32x4 xv[4][8];
; #pragma unroll
;                 for (int rr = 0; rr < 4; ++rr)
; #pragma unroll
;                     for (int j = 0; j < 8; ++j) { const size_t o0 = (size_t)(m0 + rr) * D + 4 * lq + 256 * j;
;                         if (l == 0) xv[rr][j] = __builtin_nontemporal_load((const GAS f32x4*)(Fx + o0)); else { const v2u a = __builtin_nontemporal_load((const GAS v2u*)(Xb + o0)); xv[rr][j] = bf4(a.x, a.y); } }
; #pragma unroll
;                 for (int j = 0; j < 8; ++j) { const int k = 4 * lq + 256 * j;
;                     const f32x4 sh = *(const GAS f32x4*)(mrow + k), sc = *(const GAS f32x4*)(mrow + 2048 + k) + 1.0f;
; #pragma unroll
;                     for (int rr = 0; rr < 4; ++rr) { const int rloc = 4 * F.wave + rr; const f32x4 h = xv[rr][j] * sc + sh;
;                         v2u o; o.x = pk2(h.x, h.y); o.y = pk2(h.z, h.w);
;                         *(GAS v2u*)(hbuf + (size_t)(m0 + rr) * D + k) = o;
;                         const int chunk = (lq >> 1) + 32 * j;
;                         *(LAS v2u*)(hs + rloc * 4096 + ((chunk ^ (rloc & 15)) << 4) + (lq & 1) * 8) = o; } }
.LBB0_1048:
	s_xor_b32 s18, s16, 63
	s_and_b64 s[16:17], s[10:11], exec
	s_cselect_b32 s16, s18, s40
	s_lshl_b32 s51, s16, 5
	s_add_i32 s22, s51, s25
	s_ashr_i32 s16, s22, 11
	s_add_i32 s16, s16, 8
	s_ashr_i32 s23, s22, 31
	s_mul_hi_i32 s33, s16, 0xc000
	s_mul_i32 s52, s16, 0xc000
	s_lshl_b64 s[20:21], s[22:23], 12
	s_or_b32 s16, s22, 1
	s_or_b32 s18, s22, 2
	s_or_b32 s22, s22, 3
	v_mov_b32_e32 v82, v79
	s_ashr_i32 s17, s16, 31
	s_ashr_i32 s19, s18, 31
	s_ashr_i32 s23, s22, 31
	s_lshl_b64 s[16:17], s[16:17], 12
	v_lshlrev_b32_e32 v0, 2, v82
	s_lshl_b64 s[18:19], s[18:19], 12
	s_lshl_b64 s[22:23], s[22:23], 12
	v_ashrrev_i32_e32 v1, 31, v0
	s_add_u32 s52, s3, s52
	v_lshlrev_b64 v[6:7], 1, v[0:1]
	s_addc_u32 s53, s24, s33
	v_lshl_add_u64 v[2:3], s[6:7], 0, v[6:7]
	v_lshl_add_u64 v[42:43], v[0:1], 2, s[52:53]
	v_lshl_add_u64 v[20:21], v[2:3], 0, s[20:21]
	v_add_co_u32_e32 v8, vcc, s45, v42
	global_load_dwordx2 v[10:11], v[20:21], off nt
	v_lshl_add_u64 v[22:23], v[2:3], 0, s[16:17]
	v_lshl_add_u64 v[28:29], v[2:3], 0, s[18:19]
	v_lshl_add_u64 v[38:39], v[2:3], 0, s[22:23]
	v_addc_co_u32_e32 v9, vcc, 0, v43, vcc
	global_load_dwordx2 v[12:13], v[22:23], off nt
	global_load_dwordx2 v[14:15], v[28:29], off nt
	global_load_dwordx2 v[18:19], v[38:39], off nt
	ds_read_b128 v[2:5], v252 offset:8192
	ds_read_b128 v[24:27], v252 offset:0
	v_lshl_add_u64 v[6:7], s[8:9], 0, v[6:7]
	v_lshl_add_u64 v[0:1], v[6:7], 0, s[20:21]
	global_load_dwordx2 v[30:31], v[20:21], off offset:512 nt
	global_load_dwordx2 v[44:45], v[20:21], off offset:1024 nt
	global_load_dwordx2 v[52:53], v[20:21], off offset:1536 nt
	global_load_dwordx2 v[32:33], v[22:23], off offset:512 nt
	global_load_dwordx2 v[40:41], v[22:23], off offset:1024 nt
	global_load_dwordx2 v[50:51], v[22:23], off offset:1536 nt
	global_load_dwordx2 v[60:61], v[28:29], off offset:512 nt
	global_load_dwordx2 v[36:37], v[28:29], off offset:1024 nt
	global_load_dwordx2 v[48:49], v[28:29], off offset:1536 nt
	global_load_dwordx2 v[62:63], v[38:39], off offset:512 nt
	global_load_dwordx2 v[34:35], v[38:39], off offset:1024 nt
	global_load_dwordx2 v[46:47], v[38:39], off offset:1536 nt
	v_lshl_add_u64 v[54:55], v[42:43], 0, s[14:15]
	v_lshlrev_b32_e32 v108, 3, v82
	v_and_b32_e32 v108, 8, v108
	v_ashrrev_i32_e32 v156, 5, v82
	v_add_u32_e32 v158, s36, v156
	s_waitcnt vmcnt(15) lgkmcnt(0)
	v_lshlrev_b32_e32 v56, 16, v10
	v_and_b32_e32 v57, 0xffff0000, v10
	v_lshlrev_b32_e32 v10, 16, v11
	v_and_b32_e32 v11, 0xffff0000, v11
	s_waitcnt vmcnt(14)
	v_lshlrev_b32_e32 v58, 16, v12
	v_and_b32_e32 v59, 0xffff0000, v12
	s_waitcnt vmcnt(12)
	v_pk_add_f32 v[68:69], v[4:5], 1.0 op_sel_hi:[1,0]
	v_pk_add_f32 v[70:71], v[2:3], 1.0 op_sel_hi:[1,0]
	v_lshlrev_b32_e32 v12, 16, v13
	v_and_b32_e32 v13, 0xffff0000, v13
	v_pk_fma_f32 v[2:3], v[68:69], v[10:11], v[26:27]
	v_pk_fma_f32 v[4:5], v[70:71], v[56:57], v[24:25]
	v_pk_fma_f32 v[56:57], v[68:69], v[12:13], v[26:27]
	v_pk_fma_f32 v[10:11], v[70:71], v[58:59], v[24:25]
	v_bfe_u32 v12, v4, 16, 1
	v_bfe_u32 v58, v2, 16, 1
	v_bfe_u32 v13, v5, 16, 1
	v_bfe_u32 v59, v3, 16, 1
	v_add3_u32 v4, v4, v12, s43
	v_add3_u32 v2, v2, v58, s43
	v_lshlrev_b32_e32 v64, 16, v14
	v_and_b32_e32 v65, 0xffff0000, v14
	v_lshlrev_b32_e32 v14, 16, v15
	v_and_b32_e32 v15, 0xffff0000, v15
	v_lshlrev_b32_e32 v66, 16, v18
	v_and_b32_e32 v67, 0xffff0000, v18
	v_lshlrev_b32_e32 v18, 16, v19
	v_and_b32_e32 v19, 0xffff0000, v19
	v_add3_u32 v5, v5, v13, s43
	v_add3_u32 v3, v3, v59, s43
	v_lshrrev_b32_e32 v4, 16, v4
	v_lshrrev_b32_e32 v2, 16, v2
	v_and_or_b32 v12, v5, s41, v4
	v_and_or_b32 v13, v3, s41, v2
	v_bfe_u32 v2, v56, 16, 1
	v_pk_fma_f32 v[4:5], v[68:69], v[14:15], v[26:27]
	v_pk_fma_f32 v[14:15], v[70:71], v[64:65], v[24:25]
	v_pk_fma_f32 v[26:27], v[68:69], v[18:19], v[26:27]
	v_pk_fma_f32 v[18:19], v[70:71], v[66:67], v[24:25]
	v_add3_u32 v2, v56, v2, s43
	v_bfe_u32 v56, v14, 16, 1
	v_bfe_u32 v24, v18, 16, 1
	v_add3_u32 v14, v14, v56, s43
	v_bfe_u32 v56, v15, 16, 1
	v_add3_u32 v18, v18, v24, s43
	v_bfe_u32 v24, v19, 16, 1
	v_lshrrev_b32_e32 v14, 16, v14
	v_add3_u32 v15, v15, v56, s43
	v_lshrrev_b32_e32 v18, 16, v18
	v_add3_u32 v19, v19, v24, s43
	v_bfe_u32 v72, v10, 16, 1
	v_and_or_b32 v14, v15, s41, v14
	v_bfe_u32 v15, v4, 16, 1
	v_and_or_b32 v18, v19, s41, v18
	v_bfe_u32 v19, v26, 16, 1
	v_bfe_u32 v73, v11, 16, 1
	v_add3_u32 v10, v10, v72, s43
	v_bfe_u32 v3, v57, 16, 1
	v_add3_u32 v4, v4, v15, s43
	v_bfe_u32 v15, v5, 16, 1
	v_add3_u32 v19, v26, v19, s43
	v_bfe_u32 v24, v27, 16, 1
	v_add3_u32 v11, v11, v73, s43
	v_lshrrev_b32_e32 v10, 16, v10
	v_lshrrev_b32_e32 v2, 16, v2
	v_add3_u32 v3, v57, v3, s43
	v_lshrrev_b32_e32 v4, 16, v4
	v_add3_u32 v5, v5, v15, s43
	v_lshrrev_b32_e32 v19, 16, v19
	v_add3_u32 v24, v27, v24, s43
	v_and_or_b32 v10, v11, s41, v10
	v_and_or_b32 v11, v3, s41, v2
	v_lshl_add_u64 v[2:3], v[6:7], 0, s[16:17]
	v_and_or_b32 v15, v5, s41, v4
	v_lshl_add_u64 v[4:5], v[6:7], 0, s[18:19]
	v_and_or_b32 v19, v24, s41, v19
	v_lshl_add_u64 v[6:7], v[6:7], 0, s[22:23]
	global_store_dwordx2 v[0:1], v[12:13], off
	global_store_dwordx2 v[2:3], v[10:11], off
	global_store_dwordx2 v[4:5], v[14:15], off
	global_store_dwordx2 v[6:7], v[18:19], off
	ds_read_b128 v[24:27], v252 offset:9216
	ds_read_b128 v[56:59], v252 offset:1024
	s_waitcnt vmcnt(15) lgkmcnt(0)
	v_lshlrev_b32_e32 v64, 16, v30
	v_and_b32_e32 v65, 0xffff0000, v30
	v_lshlrev_b32_e32 v30, 16, v31
	v_and_b32_e32 v31, 0xffff0000, v31
	s_waitcnt vmcnt(12)
	v_lshlrev_b32_e32 v66, 16, v32
	v_and_b32_e32 v67, 0xffff0000, v32
	v_lshlrev_b32_e32 v32, 16, v33
	v_and_b32_e32 v33, 0xffff0000, v33
	s_waitcnt vmcnt(9)
; #define GAS __attribute__((address_space(1)))
; #define LAS __attribute__((address_space(3)))
; __device__ __forceinline__ unsigned pk2(float lo, float hi) { return f2bf(lo) | (f2bf(hi) << 16); }
; __device__ __forceinline__ f32x4 bf4(unsigned a, unsigned b) { return (f32x4){bflo(a), bfhi(a), bflo(b), bfhi(b)}; }
; template <int l>
; __device__ __forceinline__ void layer_phases(Frame& F, const XcdBarrier& bar, const int lo, const int hi) {
;     ...
;                 f32x4 xv[4][8];
; #pragma unroll
;                 for (int rr = 0; rr < 4; ++rr)
; #pragma unroll
;                     for (int j = 0; j < 8; ++j) { const size_t o0 = (size_t)(m0 + rr) * D + 4 * lq + 256 * j;
;                         if (l == 0) xv[rr][j] = __builtin_nontemporal_load((const GAS f32x4*)(Fx + o0)); else { const v2u a = __builtin_nontemporal_load((const GAS v2u*)(Xb + o0)); xv[rr][j] = bf4(a.x, a.y); } }
; #pragma unroll
;                 for (int j = 0; j < 8; ++j) { const int k = 4 * lq + 256 * j;
;                     const f32x4 sh = *(const GAS f32x4*)(mrow + k), sc = *(const GAS f32x4*)(mrow + 2048 + k) + 1.0f;
; #pragma unroll
;                     for (int rr = 0; rr < 4; ++rr) { const int rloc = 4 * F.wave + rr; const f32x4 h = xv[rr][j] * sc + sh;
;                         v2u o; o.x = pk2(h.x, h.y); o.y = pk2(h.z, h.w);
;                         *(GAS v2u*)(hbuf + (size_t)(m0 + rr) * D + k) = o;
;                         const int chunk = (lq >> 1) + 32 * j;
;                         *(LAS v2u*)(hs + rloc * 4096 + ((chunk ^ (rloc & 15)) << 4) + (lq & 1) * 8) = o; } }
	v_lshlrev_b32_e32 v68, 16, v60
	v_and_b32_e32 v69, 0xffff0000, v60
	v_lshlrev_b32_e32 v60, 16, v61
	v_and_b32_e32 v61, 0xffff0000, v61
	s_waitcnt vmcnt(6)
	v_lshlrev_b32_e32 v70, 16, v62
	v_and_b32_e32 v71, 0xffff0000, v62
	v_lshlrev_b32_e32 v62, 16, v63
	v_and_b32_e32 v63, 0xffff0000, v63
	s_waitcnt vmcnt(4)
	v_pk_add_f32 v[72:73], v[26:27], 1.0 op_sel_hi:[1,0]
	v_pk_add_f32 v[74:75], v[24:25], 1.0 op_sel_hi:[1,0]
	v_pk_fma_f32 v[24:25], v[72:73], v[30:31], v[58:59]
	v_pk_fma_f32 v[26:27], v[74:75], v[64:65], v[56:57]
	v_pk_fma_f32 v[30:31], v[72:73], v[32:33], v[58:59]
	v_pk_fma_f32 v[32:33], v[74:75], v[66:67], v[56:57]
	v_bfe_u32 v64, v26, 16, 1
	v_bfe_u32 v66, v24, 16, 1
	v_bfe_u32 v65, v27, 16, 1
	v_bfe_u32 v67, v25, 16, 1
	v_bfe_u32 v83, v30, 16, 1
	v_add3_u32 v26, v26, v64, s43
	v_add3_u32 v24, v24, v66, s43
	v_bfe_u32 v76, v32, 16, 1
	v_bfe_u32 v84, v31, 16, 1
	v_add3_u32 v27, v27, v65, s43
	v_add3_u32 v25, v25, v67, s43
	v_add3_u32 v30, v30, v83, s43
	v_lshrrev_b32_e32 v26, 16, v26
	v_lshrrev_b32_e32 v24, 16, v24
	v_bfe_u32 v77, v33, 16, 1
	v_add3_u32 v32, v32, v76, s43
	v_lshrrev_b32_e32 v30, 16, v30
	v_and_or_b32 v26, v27, s41, v26
	v_and_or_b32 v27, v25, s41, v24
	v_add3_u32 v25, v31, v84, s43
	v_add3_u32 v33, v33, v77, s43
	v_lshrrev_b32_e32 v32, 16, v32
	v_and_or_b32 v25, v25, s41, v30
	v_pk_fma_f32 v[30:31], v[74:75], v[68:69], v[56:57]
	v_and_or_b32 v24, v33, s41, v32
	v_pk_fma_f32 v[32:33], v[72:73], v[60:61], v[58:59]
	v_bfe_u32 v60, v30, 16, 1
	v_add3_u32 v30, v30, v60, s43
	v_bfe_u32 v60, v31, 16, 1
	v_lshrrev_b32_e32 v30, 16, v30
	v_add3_u32 v31, v31, v60, s43
	v_and_or_b32 v30, v31, s41, v30
	v_bfe_u32 v31, v32, 16, 1
	v_add3_u32 v31, v32, v31, s43
	v_bfe_u32 v32, v33, 16, 1
	v_lshrrev_b32_e32 v31, 16, v31
	v_add3_u32 v32, v33, v32, s43
	v_and_or_b32 v31, v32, s41, v31
	v_pk_fma_f32 v[32:33], v[74:75], v[70:71], v[56:57]
	v_pk_fma_f32 v[58:59], v[72:73], v[62:63], v[58:59]
	v_bfe_u32 v56, v32, 16, 1
	v_add3_u32 v32, v32, v56, s43
	v_bfe_u32 v56, v33, 16, 1
	v_lshrrev_b32_e32 v32, 16, v32
	v_add3_u32 v33, v33, v56, s43
	v_and_or_b32 v32, v33, s41, v32
	v_bfe_u32 v33, v58, 16, 1
	v_add3_u32 v33, v58, v33, s43
	v_bfe_u32 v56, v59, 16, 1
	v_lshrrev_b32_e32 v33, 16, v33
	v_add3_u32 v56, v59, v56, s43
	v_and_or_b32 v33, v56, s41, v33
	global_store_dwordx2 v[0:1], v[26:27], off offset:512
	global_store_dwordx2 v[2:3], v[24:25], off offset:512
	global_store_dwordx2 v[4:5], v[30:31], off offset:512
	global_store_dwordx2 v[6:7], v[32:33], off offset:512
	ds_read_b128 v[56:59], v252 offset:10240
	ds_read_b128 v[60:63], v252 offset:2048
	v_lshlrev_b32_e32 v64, 16, v44
	v_and_b32_e32 v65, 0xffff0000, v44
	v_lshlrev_b32_e32 v44, 16, v45
	v_and_b32_e32 v45, 0xffff0000, v45
	v_lshlrev_b32_e32 v66, 16, v40
	v_and_b32_e32 v67, 0xffff0000, v40
	v_lshlrev_b32_e32 v40, 16, v41
	v_and_b32_e32 v41, 0xffff0000, v41
	v_lshlrev_b32_e32 v68, 16, v36
	v_and_b32_e32 v69, 0xffff0000, v36
	v_lshlrev_b32_e32 v36, 16, v37
	v_and_b32_e32 v37, 0xffff0000, v37
	v_lshlrev_b32_e32 v70, 16, v34
	v_and_b32_e32 v71, 0xffff0000, v34
	v_lshlrev_b32_e32 v72, 16, v35
	v_and_b32_e32 v73, 0xffff0000, v35
	s_waitcnt lgkmcnt(0)
	v_pk_add_f32 v[58:59], v[58:59], 1.0 op_sel_hi:[1,0]
	v_pk_add_f32 v[56:57], v[56:57], 1.0 op_sel_hi:[1,0]
	v_pk_fma_f32 v[34:35], v[58:59], v[44:45], v[62:63]
	v_pk_fma_f32 v[44:45], v[56:57], v[64:65], v[60:61]
	v_pk_fma_f32 v[40:41], v[58:59], v[40:41], v[62:63]
	v_pk_fma_f32 v[64:65], v[56:57], v[66:67], v[60:61]
	v_pk_fma_f32 v[66:67], v[58:59], v[36:37], v[62:63]
	v_pk_fma_f32 v[36:37], v[56:57], v[68:69], v[60:61]
	v_bfe_u32 v68, v44, 16, 1
	v_bfe_u32 v74, v34, 16, 1
	v_bfe_u32 v83, v40, 16, 1
	v_bfe_u32 v69, v45, 16, 1
	v_bfe_u32 v75, v35, 16, 1
	v_bfe_u32 v84, v41, 16, 1
	v_add3_u32 v44, v44, v68, s43
	v_add3_u32 v34, v34, v74, s43
	v_add3_u32 v40, v40, v83, s43
	v_bfe_u32 v85, v36, 16, 1
	v_add3_u32 v45, v45, v69, s43
	v_add3_u32 v35, v35, v75, s43
	v_add3_u32 v41, v41, v84, s43
	v_lshrrev_b32_e32 v44, 16, v44
	v_lshrrev_b32_e32 v34, 16, v34
	v_lshrrev_b32_e32 v40, 16, v40
	v_add3_u32 v36, v36, v85, s43
	v_and_or_b32 v44, v45, s41, v44
	v_and_or_b32 v45, v35, s41, v34
	v_and_or_b32 v35, v41, s41, v40
	v_bfe_u32 v40, v37, 16, 1
	v_lshrrev_b32_e32 v36, 16, v36
	v_add3_u32 v37, v37, v40, s43
	v_and_or_b32 v36, v37, s41, v36
	v_bfe_u32 v37, v66, 16, 1
	v_add3_u32 v37, v66, v37, s43
	v_bfe_u32 v40, v67, 16, 1
	v_lshrrev_b32_e32 v37, 16, v37
	v_add3_u32 v40, v67, v40, s43
	v_and_or_b32 v37, v40, s41, v37
	v_pk_fma_f32 v[40:41], v[56:57], v[70:71], v[60:61]
	v_pk_fma_f32 v[58:59], v[58:59], v[72:73], v[62:63]
	v_bfe_u32 v56, v40, 16, 1
	v_add3_u32 v40, v40, v56, s43
	v_bfe_u32 v56, v41, 16, 1
	v_lshrrev_b32_e32 v40, 16, v40
	v_add3_u32 v41, v41, v56, s43
	v_and_or_b32 v40, v41, s41, v40
	v_bfe_u32 v41, v58, 16, 1
	v_bfe_u32 v76, v64, 16, 1
	v_add3_u32 v41, v58, v41, s43
	v_bfe_u32 v56, v59, 16, 1
	v_bfe_u32 v77, v65, 16, 1
	v_add3_u32 v64, v64, v76, s43
	v_lshrrev_b32_e32 v41, 16, v41
	v_add3_u32 v56, v59, v56, s43
	v_add3_u32 v65, v65, v77, s43
	v_lshrrev_b32_e32 v64, 16, v64
	v_and_or_b32 v41, v56, s41, v41
	v_and_or_b32 v34, v65, s41, v64
	global_store_dwordx2 v[0:1], v[44:45], off offset:1024
	global_store_dwordx2 v[2:3], v[34:35], off offset:1024
	global_store_dwordx2 v[4:5], v[36:37], off offset:1024
	global_store_dwordx2 v[6:7], v[40:41], off offset:1024
	ds_read_b128 v[54:57], v252 offset:11264
	s_nop 0
	ds_read_b128 v[58:61], v252 offset:3072
	global_load_dwordx2 v[84:85], v[20:21], off offset:2048 nt
	global_load_dwordx2 v[86:87], v[22:23], off offset:2048 nt
	global_load_dwordx2 v[88:89], v[28:29], off offset:2048 nt
	global_load_dwordx2 v[90:91], v[38:39], off offset:2048 nt
	v_lshlrev_b32_e32 v62, 16, v52
	v_and_b32_e32 v63, 0xffff0000, v52
	v_lshlrev_b32_e32 v52, 16, v53
	v_and_b32_e32 v53, 0xffff0000, v53
	v_lshlrev_b32_e32 v64, 16, v50
	v_and_b32_e32 v65, 0xffff0000, v50
	v_lshlrev_b32_e32 v68, 16, v46
	v_and_b32_e32 v69, 0xffff0000, v46
	v_lshlrev_b32_e32 v70, 16, v47
	v_and_b32_e32 v71, 0xffff0000, v47
	v_lshlrev_b32_e32 v50, 16, v51
	v_and_b32_e32 v51, 0xffff0000, v51
	v_lshlrev_b32_e32 v66, 16, v48
	v_and_b32_e32 v67, 0xffff0000, v48
	v_lshlrev_b32_e32 v48, 16, v49
	v_and_b32_e32 v49, 0xffff0000, v49
	v_add_co_u32_e32 v42, vcc, s44, v42
	s_waitcnt lgkmcnt(0)
; #define GAS __attribute__((address_space(1)))
; #define LAS __attribute__((address_space(3)))
; __device__ __forceinline__ unsigned pk2(float lo, float hi) { return f2bf(lo) | (f2bf(hi) << 16); }
; __device__ __forceinline__ f32x4 bf4(unsigned a, unsigned b) { return (f32x4){bflo(a), bfhi(a), bflo(b), bfhi(b)}; }
; template <int l>
; __device__ __forceinline__ void layer_phases(Frame& F, const XcdBarrier& bar, const int lo, const int hi) {
;     ...
;                 f32x4 xv[4][8];
; #pragma unroll
;                 for (int rr = 0; rr < 4; ++rr)
; #pragma unroll
;                     for (int j = 0; j < 8; ++j) { const size_t o0 = (size_t)(m0 + rr) * D + 4 * lq + 256 * j;
;                         if (l == 0) xv[rr][j] = __builtin_nontemporal_load((const GAS f32x4*)(Fx + o0)); else { const v2u a = __builtin_nontemporal_load((const GAS v2u*)(Xb + o0)); xv[rr][j] = bf4(a.x, a.y); } }
; #pragma unroll
;                 for (int j = 0; j < 8; ++j) { const int k = 4 * lq + 256 * j;
;                     const f32x4 sh = *(const GAS f32x4*)(mrow + k), sc = *(const GAS f32x4*)(mrow + 2048 + k) + 1.0f;
; #pragma unroll
;                     for (int rr = 0; rr < 4; ++rr) { const int rloc = 4 * F.wave + rr; const f32x4 h = xv[rr][j] * sc + sh;
;                         v2u o; o.x = pk2(h.x, h.y); o.y = pk2(h.z, h.w);
;                         *(GAS v2u*)(hbuf + (size_t)(m0 + rr) * D + k) = o;
;                         const int chunk = (lq >> 1) + 32 * j;
;                         *(LAS v2u*)(hs + rloc * 4096 + ((chunk ^ (rloc & 15)) << 4) + (lq & 1) * 8) = o; } }
	v_pk_add_f32 v[56:57], v[56:57], 1.0 op_sel_hi:[1,0]
	v_pk_add_f32 v[54:55], v[54:55], 1.0 op_sel_hi:[1,0]
	v_pk_fma_f32 v[46:47], v[56:57], v[52:53], v[60:61]
	v_pk_fma_f32 v[52:53], v[54:55], v[62:63], v[58:59]
	v_pk_fma_f32 v[62:63], v[54:55], v[64:65], v[58:59]
	v_bfe_u32 v72, v46, 16, 1
	v_pk_fma_f32 v[50:51], v[56:57], v[50:51], v[60:61]
	v_pk_fma_f32 v[64:65], v[56:57], v[48:49], v[60:61]
	v_pk_fma_f32 v[48:49], v[54:55], v[66:67], v[58:59]
	v_bfe_u32 v66, v52, 16, 1
	v_bfe_u32 v73, v47, 16, 1
	v_bfe_u32 v74, v62, 16, 1
	v_add3_u32 v46, v46, v72, s43
	v_bfe_u32 v67, v53, 16, 1
	v_bfe_u32 v75, v63, 16, 1
	v_bfe_u32 v77, v51, 16, 1
	v_bfe_u32 v83, v48, 16, 1
	v_bfe_u32 v92, v49, 16, 1
	v_add3_u32 v52, v52, v66, s43
	v_add3_u32 v47, v47, v73, s43
	v_add3_u32 v62, v62, v74, s43
	v_lshrrev_b32_e32 v46, 16, v46
	v_add3_u32 v53, v53, v67, s43
	v_add3_u32 v63, v63, v75, s43
	v_add3_u32 v66, v51, v77, s43
	v_add3_u32 v48, v48, v83, s43
	v_add3_u32 v67, v49, v92, s43
	v_lshrrev_b32_e32 v49, 16, v52
	v_lshrrev_b32_e32 v52, 16, v62
	v_and_or_b32 v51, v47, s41, v46
	v_bfe_u32 v47, v64, 16, 1
	v_bfe_u32 v76, v50, 16, 1
	v_lshrrev_b32_e32 v72, 16, v48
	v_and_or_b32 v48, v63, s41, v52
	v_add3_u32 v47, v64, v47, s43
	v_bfe_u32 v52, v65, 16, 1
	v_add3_u32 v50, v50, v76, s43
	v_lshrrev_b32_e32 v47, 16, v47
	v_add3_u32 v52, v65, v52, s43
	v_lshrrev_b32_e32 v62, 16, v50
	v_and_or_b32 v50, v53, s41, v49
	v_and_or_b32 v47, v52, s41, v47
	v_pk_fma_f32 v[52:53], v[54:55], v[68:69], v[58:59]
	v_pk_fma_f32 v[56:57], v[56:57], v[70:71], v[60:61]
	v_bfe_u32 v54, v52, 16, 1
	v_add3_u32 v52, v52, v54, s43
	v_bfe_u32 v54, v53, 16, 1
	v_lshrrev_b32_e32 v52, 16, v52
	v_add3_u32 v53, v53, v54, s43
	v_and_or_b32 v52, v53, s41, v52
	v_bfe_u32 v53, v56, 16, 1
	v_add3_u32 v53, v56, v53, s43
	v_bfe_u32 v54, v57, 16, 1
	v_lshrrev_b32_e32 v53, 16, v53
	v_add3_u32 v54, v57, v54, s43
	v_and_or_b32 v46, v67, s41, v72
	v_and_or_b32 v53, v54, s41, v53
	v_and_or_b32 v49, v66, s41, v62
	global_store_dwordx2 v[0:1], v[50:51], off offset:1536
	global_store_dwordx2 v[2:3], v[48:49], off offset:1536
	global_store_dwordx2 v[4:5], v[46:47], off offset:1536
	global_store_dwordx2 v[6:7], v[52:53], off offset:1536
	ds_read_b128 v[70:73], v252 offset:12288
	v_addc_co_u32_e32 v43, vcc, 0, v43, vcc
	ds_read_b128 v[74:77], v252 offset:4096
	global_load_dwordx2 v[92:93], v[20:21], off offset:2560 nt
	global_load_dwordx2 v[68:69], v[20:21], off offset:3072 nt
	global_load_dwordx2 v[66:67], v[20:21], off offset:3584 nt
	global_load_dwordx2 v[94:95], v[22:23], off offset:2560 nt
	global_load_dwordx2 v[64:65], v[22:23], off offset:3072 nt
	global_load_dwordx2 v[62:63], v[22:23], off offset:3584 nt
	global_load_dwordx2 v[96:97], v[28:29], off offset:2560 nt
	global_load_dwordx2 v[60:61], v[28:29], off offset:3072 nt
	global_load_dwordx2 v[58:59], v[28:29], off offset:3584 nt
	global_load_dwordx2 v[98:99], v[38:39], off offset:2560 nt
	global_load_dwordx2 v[56:57], v[38:39], off offset:3072 nt
	global_load_dwordx2 v[54:55], v[38:39], off offset:3584 nt
	s_waitcnt vmcnt(19) lgkmcnt(0)
	v_lshlrev_b32_e32 v20, 16, v84
	v_and_b32_e32 v21, 0xffff0000, v84
	s_waitcnt vmcnt(18)
	v_lshlrev_b32_e32 v28, 16, v86
	v_and_b32_e32 v29, 0xffff0000, v86
	v_lshlrev_b32_e32 v22, 16, v85
	v_and_b32_e32 v23, 0xffff0000, v85
	v_lshlrev_b32_e32 v38, 16, v87
	v_and_b32_e32 v39, 0xffff0000, v87
	s_waitcnt vmcnt(17)
	v_lshlrev_b32_e32 v84, 16, v88
	v_and_b32_e32 v85, 0xffff0000, v88
	v_lshlrev_b32_e32 v86, 16, v89
	v_and_b32_e32 v87, 0xffff0000, v89
	s_waitcnt vmcnt(16)
	v_lshlrev_b32_e32 v88, 16, v90
	v_and_b32_e32 v89, 0xffff0000, v90
	v_lshlrev_b32_e32 v90, 16, v91
	v_and_b32_e32 v91, 0xffff0000, v91
	v_pk_add_f32 v[70:71], v[70:71], 1.0 op_sel_hi:[1,0]
	v_pk_add_f32 v[72:73], v[72:73], 1.0 op_sel_hi:[1,0]
	v_pk_fma_f32 v[20:21], v[70:71], v[20:21], v[74:75]
	v_pk_fma_f32 v[28:29], v[70:71], v[28:29], v[74:75]
	v_pk_fma_f32 v[22:23], v[72:73], v[22:23], v[76:77]
	v_bfe_u32 v83, v20, 16, 1
	v_bfe_u32 v103, v28, 16, 1
	v_bfe_u32 v100, v21, 16, 1
	v_bfe_u32 v101, v22, 16, 1
	v_bfe_u32 v104, v29, 16, 1
	v_add3_u32 v20, v20, v83, s43
	v_add3_u32 v28, v28, v103, s43
	v_pk_fma_f32 v[38:39], v[72:73], v[38:39], v[76:77]
	v_bfe_u32 v102, v23, 16, 1
	v_add3_u32 v21, v21, v100, s43
	v_add3_u32 v22, v22, v101, s43
	v_add3_u32 v29, v29, v104, s43
	v_lshrrev_b32_e32 v20, 16, v20
	v_lshrrev_b32_e32 v28, 16, v28
	v_bfe_u32 v105, v38, 16, 1
	v_add3_u32 v23, v23, v102, s43
	v_lshrrev_b32_e32 v83, 16, v22
	v_and_or_b32 v22, v21, s41, v20
	v_and_or_b32 v20, v29, s41, v28
	v_pk_fma_f32 v[28:29], v[70:71], v[84:85], v[74:75]
	v_bfe_u32 v106, v39, 16, 1
	v_add3_u32 v38, v38, v105, s43
	v_and_or_b32 v23, v23, s41, v83
	v_bfe_u32 v83, v28, 16, 1
	v_add3_u32 v39, v39, v106, s43
	v_lshrrev_b32_e32 v38, 16, v38
	v_add3_u32 v28, v28, v83, s43
	v_bfe_u32 v83, v29, 16, 1
	v_and_or_b32 v21, v39, s41, v38
	v_pk_fma_f32 v[38:39], v[72:73], v[86:87], v[76:77]
	v_lshrrev_b32_e32 v28, 16, v28
	v_add3_u32 v29, v29, v83, s43
	v_and_or_b32 v28, v29, s41, v28
	v_bfe_u32 v29, v38, 16, 1
	v_add3_u32 v29, v38, v29, s43
	v_bfe_u32 v38, v39, 16, 1
	v_lshrrev_b32_e32 v29, 16, v29
	v_add3_u32 v38, v39, v38, s43
	v_and_or_b32 v29, v38, s41, v29
	v_pk_fma_f32 v[38:39], v[70:71], v[88:89], v[74:75]
	v_pk_fma_f32 v[72:73], v[72:73], v[90:91], v[76:77]
	v_bfe_u32 v70, v38, 16, 1
	v_add3_u32 v38, v38, v70, s43
	v_bfe_u32 v70, v39, 16, 1
	v_lshrrev_b32_e32 v38, 16, v38
	v_add3_u32 v39, v39, v70, s43
	v_and_or_b32 v38, v39, s41, v38
	v_bfe_u32 v39, v72, 16, 1
	v_add3_u32 v39, v72, v39, s43
	v_bfe_u32 v70, v73, 16, 1
	v_lshrrev_b32_e32 v39, 16, v39
	v_add3_u32 v70, v73, v70, s43
	v_and_or_b32 v39, v70, s41, v39
	global_store_dwordx2 v[0:1], v[22:23], off offset:2048
	global_store_dwordx2 v[2:3], v[20:21], off offset:2048
	global_store_dwordx2 v[4:5], v[28:29], off offset:2048
	global_store_dwordx2 v[6:7], v[38:39], off offset:2048
	ds_read_b128 v[70:73], v252 offset:13312
	ds_read_b128 v[84:87], v252 offset:5120
	s_waitcnt vmcnt(15) lgkmcnt(0)
; #define GAS __attribute__((address_space(1)))
; #define LAS __attribute__((address_space(3)))
; __device__ __forceinline__ unsigned pk2(float lo, float hi) { return f2bf(lo) | (f2bf(hi) << 16); }
; __device__ __forceinline__ f32x4 bf4(unsigned a, unsigned b) { return (f32x4){bflo(a), bfhi(a), bflo(b), bfhi(b)}; }
; template <int l>
; __device__ __forceinline__ void layer_phases(Frame& F, const XcdBarrier& bar, const int lo, const int hi) {
;     ...
;                 f32x4 xv[4][8];
; #pragma unroll
;                 for (int rr = 0; rr < 4; ++rr)
; #pragma unroll
;                     for (int j = 0; j < 8; ++j) { const size_t o0 = (size_t)(m0 + rr) * D + 4 * lq + 256 * j;
;                         if (l == 0) xv[rr][j] = __builtin_nontemporal_load((const GAS f32x4*)(Fx + o0)); else { const v2u a = __builtin_nontemporal_load((const GAS v2u*)(Xb + o0)); xv[rr][j] = bf4(a.x, a.y); } }
; #pragma unroll
;                 for (int j = 0; j < 8; ++j) { const int k = 4 * lq + 256 * j;
;                     const f32x4 sh = *(const GAS f32x4*)(mrow + k), sc = *(const GAS f32x4*)(mrow + 2048 + k) + 1.0f;
; #pragma unroll
;                     for (int rr = 0; rr < 4; ++rr) { const int rloc = 4 * F.wave + rr; const f32x4 h = xv[rr][j] * sc + sh;
;                         v2u o; o.x = pk2(h.x, h.y); o.y = pk2(h.z, h.w);
;                         *(GAS v2u*)(hbuf + (size_t)(m0 + rr) * D + k) = o;
;                         const int chunk = (lq >> 1) + 32 * j;
;                         *(LAS v2u*)(hs + rloc * 4096 + ((chunk ^ (rloc & 15)) << 4) + (lq & 1) * 8) = o; } }
	v_lshlrev_b32_e32 v74, 16, v92
	v_and_b32_e32 v75, 0xffff0000, v92
	v_lshlrev_b32_e32 v76, 16, v93
	v_and_b32_e32 v77, 0xffff0000, v93
	s_waitcnt vmcnt(12)
	v_lshlrev_b32_e32 v88, 16, v94
	v_and_b32_e32 v89, 0xffff0000, v94
	v_lshlrev_b32_e32 v90, 16, v95
	v_and_b32_e32 v91, 0xffff0000, v95
	s_waitcnt vmcnt(9)
	v_lshlrev_b32_e32 v92, 16, v96
	v_and_b32_e32 v93, 0xffff0000, v96
	v_lshlrev_b32_e32 v94, 16, v97
	v_and_b32_e32 v95, 0xffff0000, v97
	s_waitcnt vmcnt(6)
	v_lshlrev_b32_e32 v96, 16, v98
	v_and_b32_e32 v97, 0xffff0000, v98
	v_lshlrev_b32_e32 v98, 16, v99
	v_and_b32_e32 v99, 0xffff0000, v99
	s_waitcnt vmcnt(4)
	v_pk_add_f32 v[102:103], v[70:71], 1.0 op_sel_hi:[1,0]
	v_pk_add_f32 v[100:101], v[72:73], 1.0 op_sel_hi:[1,0]
	v_pk_fma_f32 v[72:73], v[102:103], v[74:75], v[84:85]
	v_pk_fma_f32 v[70:71], v[100:101], v[76:77], v[86:87]
	v_pk_fma_f32 v[74:75], v[100:101], v[90:91], v[86:87]
	v_pk_fma_f32 v[76:77], v[102:103], v[88:89], v[84:85]
	v_bfe_u32 v83, v72, 16, 1
	v_pk_fma_f32 v[88:89], v[100:101], v[94:95], v[86:87]
	v_pk_fma_f32 v[90:91], v[102:103], v[92:93], v[84:85]
	v_bfe_u32 v92, v73, 16, 1
	v_bfe_u32 v93, v70, 16, 1
	v_bfe_u32 v95, v76, 16, 1
	v_bfe_u32 v105, v74, 16, 1
	v_add3_u32 v72, v72, v83, s43
	v_bfe_u32 v94, v71, 16, 1
	v_bfe_u32 v104, v77, 16, 1
	v_bfe_u32 v106, v75, 16, 1
	v_bfe_u32 v107, v90, 16, 1
	v_add3_u32 v73, v73, v92, s43
	v_add3_u32 v70, v70, v93, s43
	v_add3_u32 v76, v76, v95, s43
	v_add3_u32 v74, v74, v105, s43
	v_lshrrev_b32_e32 v72, 16, v72
	v_add3_u32 v71, v71, v94, s43
	v_add3_u32 v77, v77, v104, s43
	v_add3_u32 v83, v75, v106, s43
	v_add3_u32 v75, v90, v107, s43
	v_lshrrev_b32_e32 v70, 16, v70
	v_lshrrev_b32_e32 v76, 16, v76
	v_lshrrev_b32_e32 v90, 16, v74
	v_and_or_b32 v74, v73, s41, v72
	v_bfe_u32 v73, v88, 16, 1
	v_lshrrev_b32_e32 v92, 16, v75
	v_and_or_b32 v75, v71, s41, v70
	v_and_or_b32 v70, v77, s41, v76
	v_add3_u32 v73, v88, v73, s43
	v_bfe_u32 v76, v89, 16, 1
	v_lshrrev_b32_e32 v73, 16, v73
	v_add3_u32 v76, v89, v76, s43
	v_and_or_b32 v73, v76, s41, v73
	v_pk_fma_f32 v[76:77], v[102:103], v[96:97], v[84:85]
	v_and_or_b32 v71, v83, s41, v90
	v_bfe_u32 v83, v76, 16, 1
	v_add3_u32 v76, v76, v83, s43
	v_bfe_u32 v83, v77, 16, 1
	v_pk_fma_f32 v[86:87], v[100:101], v[98:99], v[86:87]
	v_lshrrev_b32_e32 v76, 16, v76
	v_add3_u32 v77, v77, v83, s43
	v_and_or_b32 v76, v77, s41, v76
	v_bfe_u32 v77, v86, 16, 1
	v_bfe_u32 v72, v91, 16, 1
	v_add3_u32 v77, v86, v77, s43
	v_bfe_u32 v83, v87, 16, 1
	v_add3_u32 v72, v91, v72, s43
	v_lshrrev_b32_e32 v77, 16, v77
	v_add3_u32 v83, v87, v83, s43
	v_and_or_b32 v72, v72, s41, v92
	v_and_or_b32 v77, v83, s41, v77
	global_store_dwordx2 v[0:1], v[74:75], off offset:2560
	global_store_dwordx2 v[2:3], v[70:71], off offset:2560
	global_store_dwordx2 v[4:5], v[72:73], off offset:2560
	global_store_dwordx2 v[6:7], v[76:77], off offset:2560
	ds_read_b128 v[84:87], v252 offset:14336
	ds_read_b128 v[88:91], v252 offset:6144
	v_lshrrev_b32_e32 v83, 1, v82
	v_xor_b32_e32 v109, s27, v83
	v_lshlrev_b32_e32 v109, 4, v109
	v_add3_u32 v109, s26, v109, v108
	ds_write_b64 v109, v[12:13]
	v_xor_b32_e32 v12, s29, v83
	v_lshlrev_b32_e32 v12, 4, v12
	v_add3_u32 v12, s28, v12, v108
	ds_write_b64 v12, v[10:11]
	v_xor_b32_e32 v10, s31, v83
	v_lshlrev_b32_e32 v10, 4, v10
	v_add3_u32 v10, s30, v10, v108
	ds_write_b64 v10, v[14:15]
	v_xor_b32_e32 v10, s35, v83
	v_lshlrev_b32_e32 v10, 4, v10
	v_add3_u32 v10, s34, v10, v108
	ds_write_b64 v10, v[18:19]
	v_add_u32_e32 v10, 32, v83
	v_xor_b32_e32 v11, s27, v10
	v_lshlrev_b32_e32 v11, 4, v11
	v_add3_u32 v11, s26, v11, v108
	ds_write_b64 v11, v[26:27]
	v_xor_b32_e32 v11, s29, v10
	v_lshlrev_b32_e32 v11, 4, v11
	v_add3_u32 v11, s28, v11, v108
	ds_write_b64 v11, v[24:25]
	v_xor_b32_e32 v11, s31, v10
	v_xor_b32_e32 v10, s35, v10
	v_lshlrev_b32_e32 v11, 4, v11
	v_lshlrev_b32_e32 v10, 4, v10
	v_add3_u32 v11, s30, v11, v108
	v_add3_u32 v10, s34, v10, v108
	v_add_u32_e32 v109, 64, v83
	v_lshlrev_b32_e32 v92, 16, v68
	v_and_b32_e32 v93, 0xffff0000, v68
	ds_write_b64 v11, v[30:31]
	ds_write_b64 v10, v[32:33]
	v_xor_b32_e32 v10, s27, v109
	v_lshlrev_b32_e32 v10, 4, v10
	v_add3_u32 v10, s26, v10, v108
	v_lshlrev_b32_e32 v94, 16, v69
	v_and_b32_e32 v95, 0xffff0000, v69
	ds_write_b64 v10, v[44:45]
	v_lshlrev_b32_e32 v96, 16, v64
	v_and_b32_e32 v97, 0xffff0000, v64
	v_lshlrev_b32_e32 v98, 16, v65
	v_and_b32_e32 v99, 0xffff0000, v65
	v_lshlrev_b32_e32 v100, 16, v60
	v_and_b32_e32 v101, 0xffff0000, v60
	v_lshlrev_b32_e32 v102, 16, v61
	v_and_b32_e32 v103, 0xffff0000, v61
	v_lshlrev_b32_e32 v104, 16, v56
	v_and_b32_e32 v105, 0xffff0000, v56
	v_lshlrev_b32_e32 v106, 16, v57
	v_and_b32_e32 v107, 0xffff0000, v57
	v_xor_b32_e32 v44, s29, v109
	v_lshlrev_b32_e32 v68, 16, v66
	v_and_b32_e32 v69, 0xffff0000, v66
	v_lshlrev_b32_e32 v66, 16, v67
	v_and_b32_e32 v67, 0xffff0000, v67
	v_lshlrev_b32_e32 v64, 16, v62
	v_and_b32_e32 v65, 0xffff0000, v62
	v_lshlrev_b32_e32 v62, 16, v63
	v_and_b32_e32 v63, 0xffff0000, v63
	v_lshlrev_b32_e32 v60, 16, v58
	v_and_b32_e32 v61, 0xffff0000, v58
	v_lshlrev_b32_e32 v58, 16, v59
	v_and_b32_e32 v59, 0xffff0000, v59
	v_lshlrev_b32_e32 v56, 16, v54
	v_and_b32_e32 v57, 0xffff0000, v54
	v_lshlrev_b32_e32 v54, 16, v55
	v_and_b32_e32 v55, 0xffff0000, v55
	s_waitcnt lgkmcnt(0)
; #define GAS __attribute__((address_space(1)))
; #define LAS __attribute__((address_space(3)))
; __device__ __forceinline__ unsigned pk2(float lo, float hi) { return f2bf(lo) | (f2bf(hi) << 16); }
; __device__ __forceinline__ f32x4 bf4(unsigned a, unsigned b) { return (f32x4){bflo(a), bfhi(a), bflo(b), bfhi(b)}; }
; template <int l>
; __device__ __forceinline__ void layer_phases(Frame& F, const XcdBarrier& bar, const int lo, const int hi) {
;     ...
;                 f32x4 xv[4][8];
; #pragma unroll
;                 for (int rr = 0; rr < 4; ++rr)
; #pragma unroll
;                     for (int j = 0; j < 8; ++j) { const size_t o0 = (size_t)(m0 + rr) * D + 4 * lq + 256 * j;
;                         if (l == 0) xv[rr][j] = __builtin_nontemporal_load((const GAS f32x4*)(Fx + o0)); else { const v2u a = __builtin_nontemporal_load((const GAS v2u*)(Xb + o0)); xv[rr][j] = bf4(a.x, a.y); } }
; #pragma unroll
;                 for (int j = 0; j < 8; ++j) { const int k = 4 * lq + 256 * j;
;                     const f32x4 sh = *(const GAS f32x4*)(mrow + k), sc = *(const GAS f32x4*)(mrow + 2048 + k) + 1.0f;
; #pragma unroll
;                     for (int rr = 0; rr < 4; ++rr) { const int rloc = 4 * F.wave + rr; const f32x4 h = xv[rr][j] * sc + sh;
;                         v2u o; o.x = pk2(h.x, h.y); o.y = pk2(h.z, h.w);
;                         *(GAS v2u*)(hbuf + (size_t)(m0 + rr) * D + k) = o;
;                         const int chunk = (lq >> 1) + 32 * j;
;                         *(LAS v2u*)(hs + rloc * 4096 + ((chunk ^ (rloc & 15)) << 4) + (lq & 1) * 8) = o; } }
	v_pk_add_f32 v[12:13], v[84:85], 1.0 op_sel_hi:[1,0]
	v_pk_fma_f32 v[18:19], v[12:13], v[92:93], v[88:89]
	v_pk_add_f32 v[10:11], v[86:87], 1.0 op_sel_hi:[1,0]
	v_bfe_u32 v24, v18, 16, 1
	v_add3_u32 v18, v18, v24, s43
	v_bfe_u32 v24, v19, 16, 1
	v_pk_fma_f32 v[14:15], v[10:11], v[94:95], v[90:91]
	v_lshrrev_b32_e32 v18, 16, v18
	v_add3_u32 v19, v19, v24, s43
	v_and_or_b32 v18, v19, s41, v18
	v_bfe_u32 v19, v14, 16, 1
	v_pk_fma_f32 v[24:25], v[12:13], v[96:97], v[88:89]
	v_add3_u32 v14, v14, v19, s43
	v_bfe_u32 v19, v15, 16, 1
	v_bfe_u32 v26, v24, 16, 1
	v_lshrrev_b32_e32 v14, 16, v14
	v_add3_u32 v15, v15, v19, s43
	v_add3_u32 v24, v24, v26, s43
	v_bfe_u32 v26, v25, 16, 1
	v_and_or_b32 v19, v15, s41, v14
	v_pk_fma_f32 v[14:15], v[10:11], v[98:99], v[90:91]
	v_lshrrev_b32_e32 v24, 16, v24
	v_add3_u32 v25, v25, v26, s43
	v_and_or_b32 v30, v25, s41, v24
	v_bfe_u32 v24, v14, 16, 1
	v_add3_u32 v14, v14, v24, s43
	v_bfe_u32 v24, v15, 16, 1
	v_add3_u32 v15, v15, v24, s43
	v_pk_fma_f32 v[24:25], v[12:13], v[100:101], v[88:89]
	v_lshrrev_b32_e32 v14, 16, v14
	v_bfe_u32 v26, v24, 16, 1
	v_add3_u32 v24, v24, v26, s43
	v_bfe_u32 v26, v25, 16, 1
	v_and_or_b32 v31, v15, s41, v14
	v_pk_fma_f32 v[14:15], v[10:11], v[102:103], v[90:91]
	v_lshrrev_b32_e32 v24, 16, v24
	v_add3_u32 v25, v25, v26, s43
	v_and_or_b32 v32, v25, s41, v24
	v_bfe_u32 v24, v14, 16, 1
	v_add3_u32 v14, v14, v24, s43
	v_bfe_u32 v24, v15, 16, 1
	v_lshrrev_b32_e32 v14, 16, v14
	v_add3_u32 v15, v15, v24, s43
	v_pk_fma_f32 v[12:13], v[12:13], v[104:105], v[88:89]
	v_and_or_b32 v33, v15, s41, v14
	v_bfe_u32 v14, v12, 16, 1
	v_add3_u32 v12, v12, v14, s43
	v_bfe_u32 v14, v13, 16, 1
	v_pk_fma_f32 v[10:11], v[10:11], v[106:107], v[90:91]
	v_lshrrev_b32_e32 v12, 16, v12
	v_add3_u32 v13, v13, v14, s43
	v_and_or_b32 v14, v13, s41, v12
	v_bfe_u32 v12, v10, 16, 1
	v_add3_u32 v10, v10, v12, s43
	v_bfe_u32 v12, v11, 16, 1
	v_lshrrev_b32_e32 v10, 16, v10
	v_add3_u32 v11, v11, v12, s43
	v_and_or_b32 v15, v11, s41, v10
	global_store_dwordx2 v[0:1], v[18:19], off offset:3072
	global_store_dwordx2 v[2:3], v[30:31], off offset:3072
	global_store_dwordx2 v[4:5], v[32:33], off offset:3072
	global_store_dwordx2 v[6:7], v[14:15], off offset:3072
	ds_read_b128 v[10:13], v252 offset:7168
	ds_read_b128 v[24:27], v252 offset:15360
	v_lshlrev_b32_e32 v8, 4, v44
	v_add3_u32 v8, s28, v8, v108
	ds_write_b64 v8, v[34:35]
	v_xor_b32_e32 v8, s31, v109
	v_lshlrev_b32_e32 v8, 4, v8
	v_add3_u32 v8, s30, v8, v108
	ds_write_b64 v8, v[36:37]
	v_xor_b32_e32 v8, s35, v109
	v_lshlrev_b32_e32 v8, 4, v8
	v_add3_u32 v8, s34, v8, v108
	ds_write_b64 v8, v[40:41]
	v_add_u32_e32 v8, 0x60, v83
	v_xor_b32_e32 v9, s27, v8
	v_lshlrev_b32_e32 v9, 4, v9
	v_add3_u32 v9, s26, v9, v108
	ds_write_b64 v9, v[50:51]
	v_xor_b32_e32 v9, s29, v8
	v_lshlrev_b32_e32 v9, 4, v9
	v_add3_u32 v9, s28, v9, v108
	ds_write_b64 v9, v[48:49]
	v_xor_b32_e32 v9, s31, v8
	v_xor_b32_e32 v8, s35, v8
	v_lshlrev_b32_e32 v9, 4, v9
	v_lshlrev_b32_e32 v8, 4, v8
	v_add3_u32 v9, s30, v9, v108
	v_add3_u32 v8, s34, v8, v108
	ds_write_b64 v9, v[46:47]
	ds_write_b64 v8, v[52:53]
	v_add_u32_e32 v8, 0x80, v83
	v_xor_b32_e32 v9, s27, v8
	v_lshlrev_b32_e32 v9, 4, v9
	v_add3_u32 v9, s26, v9, v108
	ds_write_b64 v9, v[22:23]
	v_xor_b32_e32 v9, s29, v8
	v_lshlrev_b32_e32 v9, 4, v9
	v_add3_u32 v9, s28, v9, v108
	ds_write_b64 v9, v[20:21]
	v_xor_b32_e32 v9, s31, v8
	v_xor_b32_e32 v8, s35, v8
	v_lshlrev_b32_e32 v9, 4, v9
	v_lshlrev_b32_e32 v8, 4, v8
	v_add3_u32 v9, s30, v9, v108
	v_add3_u32 v8, s34, v8, v108
	ds_write_b64 v9, v[28:29]
	ds_write_b64 v8, v[38:39]
	v_add_u32_e32 v8, 0xa0, v83
	v_xor_b32_e32 v9, s27, v8
	v_lshlrev_b32_e32 v9, 4, v9
	v_add3_u32 v9, s26, v9, v108
	ds_write_b64 v9, v[74:75]
	v_xor_b32_e32 v9, s29, v8
	v_lshlrev_b32_e32 v9, 4, v9
	v_add3_u32 v9, s28, v9, v108
	ds_write_b64 v9, v[70:71]
	v_xor_b32_e32 v9, s31, v8
	v_xor_b32_e32 v8, s35, v8
	v_lshlrev_b32_e32 v9, 4, v9
	v_lshlrev_b32_e32 v8, 4, v8
	v_add3_u32 v9, s30, v9, v108
	v_add3_u32 v8, s34, v8, v108
	ds_write_b64 v9, v[72:73]
	ds_write_b64 v8, v[76:77]
	v_add_u32_e32 v8, 0xc0, v83
	v_xor_b32_e32 v9, s27, v8
	v_lshlrev_b32_e32 v9, 4, v9
	v_add3_u32 v9, s26, v9, v108
	ds_write_b64 v9, v[18:19]
	v_xor_b32_e32 v9, s29, v8
	v_lshlrev_b32_e32 v9, 4, v9
	v_add3_u32 v9, s28, v9, v108
	ds_write_b64 v9, v[30:31]
	v_xor_b32_e32 v9, s31, v8
	v_xor_b32_e32 v8, s35, v8
	v_lshlrev_b32_e32 v9, 4, v9
	v_lshlrev_b32_e32 v8, 4, v8
	v_add3_u32 v9, s30, v9, v108
	v_add3_u32 v8, s34, v8, v108
	ds_write_b64 v9, v[32:33]
	ds_write_b64 v8, v[14:15]
	s_waitcnt lgkmcnt(0)
; #define GAS __attribute__((address_space(1)))
; #define LAS __attribute__((address_space(3)))
; __device__ __forceinline__ unsigned pk2(float lo, float hi) { return f2bf(lo) | (f2bf(hi) << 16); }
; template <int l>
; __device__ __forceinline__ void layer_phases(Frame& F, const XcdBarrier& bar, const int lo, const int hi) {
;     ...
;                 for (int j = 0; j < 8; ++j) { const int k = 4 * lq + 256 * j;
;                     const f32x4 sh = *(const GAS f32x4*)(mrow + k), sc = *(const GAS f32x4*)(mrow + 2048 + k) + 1.0f;
; #pragma unroll
;                     for (int rr = 0; rr < 4; ++rr) { const int rloc = 4 * F.wave + rr; const f32x4 h = xv[rr][j] * sc + sh;
;                         v2u o; o.x = pk2(h.x, h.y); o.y = pk2(h.z, h.w);
;                         *(GAS v2u*)(hbuf + (size_t)(m0 + rr) * D + k) = o;
;                         const int chunk = (lq >> 1) + 32 * j;
;                         *(LAS v2u*)(hs + rloc * 4096 + ((chunk ^ (rloc & 15)) << 4) + (lq & 1) * 8) = o; } }
;                 asm volatile("" ::: "memory");
;                 bf16x8 bw[16][2];
;                 { const unsigned char* wb = wff + (size_t)(16 * F.wave) * 2048 + lq * 16;
; #pragma unroll
;                   for (int q = 0; q < 16; ++q) { bw[q][0] = *(const GAS bf16x8*)(wb + q * 2048); bw[q][1] = *(const GAS bf16x8*)(wb + q * 2048 + 1024); } }
	v_pk_add_f32 v[14:15], v[24:25], 1.0 op_sel_hi:[1,0]
	v_pk_add_f32 v[8:9], v[26:27], 1.0 op_sel_hi:[1,0]
	v_pk_fma_f32 v[20:21], v[14:15], v[68:69], v[10:11]
	v_pk_fma_f32 v[18:19], v[8:9], v[66:67], v[12:13]
	v_bfe_u32 v23, v20, 16, 1
	v_add3_u32 v20, v20, v23, s43
	v_bfe_u32 v23, v21, 16, 1
	v_lshrrev_b32_e32 v20, 16, v20
	v_add3_u32 v21, v21, v23, s43
	v_and_or_b32 v20, v21, s41, v20
	v_bfe_u32 v21, v18, 16, 1
	v_add3_u32 v18, v18, v21, s43
	v_bfe_u32 v21, v19, 16, 1
	v_lshrrev_b32_e32 v18, 16, v18
	v_add3_u32 v19, v19, v21, s43
	v_add_u32_e32 v22, 0xe0, v83
	v_and_or_b32 v21, v19, s41, v18
	global_store_dwordx2 v[0:1], v[20:21], off offset:3584
	v_xor_b32_e32 v0, s27, v22
	v_lshlrev_b32_e32 v0, 4, v0
	v_add3_u32 v0, s26, v0, v108
	v_pk_fma_f32 v[18:19], v[14:15], v[64:65], v[10:11]
	ds_write_b64 v0, v[20:21]
	v_bfe_u32 v20, v18, 16, 1
	v_add3_u32 v18, v18, v20, s43
	v_bfe_u32 v20, v19, 16, 1
	v_pk_fma_f32 v[0:1], v[8:9], v[62:63], v[12:13]
	v_lshrrev_b32_e32 v18, 16, v18
	v_add3_u32 v19, v19, v20, s43
	v_and_or_b32 v18, v19, s41, v18
	v_bfe_u32 v19, v0, 16, 1
	v_add3_u32 v0, v0, v19, s43
	v_bfe_u32 v19, v1, 16, 1
	v_lshrrev_b32_e32 v0, 16, v0
	v_add3_u32 v1, v1, v19, s43
	v_and_or_b32 v19, v1, s41, v0
	v_xor_b32_e32 v0, s29, v22
	v_lshlrev_b32_e32 v0, 4, v0
	global_store_dwordx2 v[2:3], v[18:19], off offset:3584
	v_add3_u32 v0, s28, v0, v108
	v_pk_fma_f32 v[2:3], v[14:15], v[60:61], v[10:11]
	ds_write_b64 v0, v[18:19]
	v_bfe_u32 v18, v2, 16, 1
	v_add3_u32 v2, v2, v18, s43
	v_bfe_u32 v18, v3, 16, 1
	v_pk_fma_f32 v[0:1], v[8:9], v[58:59], v[12:13]
	v_lshrrev_b32_e32 v2, 16, v2
	v_add3_u32 v3, v3, v18, s43
	v_and_or_b32 v2, v3, s41, v2
	v_bfe_u32 v3, v0, 16, 1
	v_add3_u32 v0, v0, v3, s43
	v_bfe_u32 v3, v1, 16, 1
	v_lshrrev_b32_e32 v0, 16, v0
	v_add3_u32 v1, v1, v3, s43
	v_and_or_b32 v3, v1, s41, v0
	v_xor_b32_e32 v0, s31, v22
	v_lshlrev_b32_e32 v0, 4, v0
	v_add3_u32 v0, s30, v0, v108
	global_store_dwordx2 v[4:5], v[2:3], off offset:3584
	ds_write_b64 v0, v[2:3]
	v_pk_fma_f32 v[2:3], v[14:15], v[56:57], v[10:11]
	v_pk_fma_f32 v[0:1], v[8:9], v[54:55], v[12:13]
	v_bfe_u32 v4, v2, 16, 1
	v_add3_u32 v2, v2, v4, s43
	v_bfe_u32 v4, v3, 16, 1
	v_lshrrev_b32_e32 v2, 16, v2
	v_add3_u32 v3, v3, v4, s43
	v_and_or_b32 v2, v3, s41, v2
	v_bfe_u32 v3, v0, 16, 1
	v_add3_u32 v0, v0, v3, s43
	v_bfe_u32 v3, v1, 16, 1
	v_lshrrev_b32_e32 v0, 16, v0
	v_add3_u32 v1, v1, v3, s43
	v_and_or_b32 v3, v1, s41, v0
	v_xor_b32_e32 v0, s35, v22
	v_lshlrev_b32_e32 v0, 4, v0
	v_add3_u32 v0, s34, v0, v108
	ds_write_b64 v0, v[2:3]
	v_lshlrev_b32_e32 v0, 4, v82
	global_store_dwordx2 v[6:7], v[2:3], off offset:3584
	v_ashrrev_i32_e32 v1, 31, v0
	v_lshl_add_u64 v[4:5], s[12:13], 0, v[0:1]
	global_load_dwordx4 v[0:3], v[4:5], off
	global_load_dwordx4 v[18:21], v[4:5], off offset:1024
	global_load_dwordx4 v[22:25], v[4:5], off offset:2048
	global_load_dwordx4 v[26:29], v[4:5], off offset:3072
	v_add_co_u32_e32 v6, vcc, s44, v4
	v_and_b32_e32 v83, 31, v82
	s_nop 0
	v_addc_co_u32_e32 v7, vcc, 0, v5, vcc
	v_add_co_u32_e32 v8, vcc, s42, v4
	v_lshl_add_u32 v157, v83, 12, 0
	s_nop 0
	v_addc_co_u32_e32 v9, vcc, 0, v5, vcc
	global_load_dwordx4 v[30:33], v[8:9], off offset:-4096
	global_load_dwordx4 v[34:37], v[6:7], off offset:1024
	global_load_dwordx4 v[38:41], v[6:7], off offset:2048
	global_load_dwordx4 v[42:45], v[8:9], off
	global_load_dwordx4 v[46:49], v[8:9], off offset:1024
	global_load_dwordx4 v[50:53], v[8:9], off offset:2048
	global_load_dwordx4 v[54:57], v[8:9], off offset:3072
	v_add_co_u32_e32 v8, vcc, s45, v4
	s_nop 1
	v_addc_co_u32_e32 v9, vcc, 0, v5, vcc
	v_add_co_u32_e32 v10, vcc, s46, v4
	s_nop 1
	v_addc_co_u32_e32 v11, vcc, 0, v5, vcc
	global_load_dwordx4 v[58:61], v[6:7], off offset:3072
	global_load_dwordx4 v[62:65], v[8:9], off offset:1024
	global_load_dwordx4 v[66:69], v[8:9], off offset:2048
	global_load_dwordx4 v[70:73], v[8:9], off offset:3072
	global_load_dwordx4 v[74:77], v[10:11], off offset:-4096
	global_load_dwordx4 v[84:87], v[10:11], off
	global_load_dwordx4 v[88:91], v[10:11], off offset:1024
	global_load_dwordx4 v[92:95], v[10:11], off offset:2048
	v_add_co_u32_e32 v6, vcc, s47, v4
	s_nop 1
	v_addc_co_u32_e32 v7, vcc, 0, v5, vcc
	v_add_co_u32_e32 v8, vcc, s48, v4
	s_nop 1
	v_addc_co_u32_e32 v9, vcc, 0, v5, vcc
	v_add_co_u32_e32 v4, vcc, s49, v4
	global_load_dwordx4 v[96:99], v[10:11], off offset:3072
	global_load_dwordx4 v[100:103], v[8:9], off offset:-4096
	global_load_dwordx4 v[104:107], v[6:7], off offset:1024
	global_load_dwordx4 v[108:111], v[6:7], off offset:2048
	global_load_dwordx4 v[112:115], v[8:9], off
	global_load_dwordx4 v[116:119], v[8:9], off offset:1024
	global_load_dwordx4 v[120:123], v[8:9], off offset:2048
	global_load_dwordx4 v[124:127], v[8:9], off offset:3072
	v_addc_co_u32_e32 v5, vcc, 0, v5, vcc
	global_load_dwordx4 v[128:131], v[6:7], off offset:3072
	global_load_dwordx4 v[132:135], v[4:5], off
	global_load_dwordx4 v[136:139], v[4:5], off offset:1024
	global_load_dwordx4 v[140:143], v[4:5], off offset:2048
	global_load_dwordx4 v[144:147], v[4:5], off offset:3072
	v_bitop3_b32 v4, v158, v82, 15 bitop3:0x78
	v_lshl_add_u32 v4, v4, 4, v157
	s_waitcnt lgkmcnt(0)
	s_barrier
; #define LAS __attribute__((address_space(3)))
; __device__ __forceinline__ int crow(int r, int hi) { return (r & 3) + 8 * (r >> 2) + 4 * hi; }
; template <int l>
; __device__ __forceinline__ void layer_phases(Frame& F, const XcdBarrier& bar, const int lo, const int hi) {
;     ...
;                 att::f32x16 acc0 = att::f32x16{};
; #pragma unroll
;                 for (int q = 0; q < 16; ++q) { const int ks = 16 * F.wave + q;
;                     const bf16x8 af = *(const LAS bf16x8*)(hs + r32 * 4096 + (((2 * ks + hi5) ^ (r32 & 15)) << 4));
;                     acc0 = __builtin_amdgcn_mfma_f32_32x32x16_bf16(af, bw[q][0], acc0, 0, 0, 0); acc0 = __builtin_amdgcn_mfma_f32_32x32x16_bf16(af, bw[q][1], acc0, 0, 0, 0); }
;                 __syncthreads();
; #pragma unroll
;                 for (int r = 0; r < 16; ++r) part[(F.wave * 32 + att::crow(r, hi5)) * 32 + r32] = acc0[r];
;                 __syncthreads();
;                 if (F.tid < 32 * NFOX) { const int row = F.tid / NFOX, j = F.tid % NFOX; float sacc = 0.f;
; #pragma unroll
;                     for (int w = 0; w < 8; ++w) sacc += part[(w * 32 + row) * 32 + j];
;                     flog[(size_t)(item * 32 + row) * 16 + j] = sacc; }
	ds_read_b128 v[148:151], v4
	v_add_u32_e32 v4, 2, v158
	v_bitop3_b32 v4, v4, v82, 15 bitop3:0x78
	v_lshl_add_u32 v4, v4, 4, v157
	ds_read_b128 v[152:155], v4
	s_waitcnt vmcnt(31) lgkmcnt(1)
	v_mfma_f32_32x32x16_bf16 v[0:15], v[148:151], v[0:3], 0
	s_waitcnt vmcnt(30)
	v_mfma_f32_32x32x16_bf16 v[0:15], v[148:151], v[18:21], v[0:15]
	v_add_u32_e32 v18, 4, v158
	v_bitop3_b32 v18, v18, v82, 15 bitop3:0x78
	v_lshl_add_u32 v18, v18, 4, v157
	ds_read_b128 v[18:21], v18
	s_waitcnt vmcnt(29) lgkmcnt(1)
	v_mfma_f32_32x32x16_bf16 v[0:15], v[152:155], v[22:25], v[0:15]
	v_add_u32_e32 v22, 6, v158
	v_bitop3_b32 v22, v22, v82, 15 bitop3:0x78
	v_lshl_add_u32 v22, v22, 4, v157
	ds_read_b128 v[22:25], v22
	s_waitcnt vmcnt(28)
	v_mfma_f32_32x32x16_bf16 v[0:15], v[152:155], v[26:29], v[0:15]
	s_waitcnt vmcnt(27) lgkmcnt(1)
	v_mfma_f32_32x32x16_bf16 v[0:15], v[18:21], v[30:33], v[0:15]
	s_waitcnt vmcnt(26)
	v_mfma_f32_32x32x16_bf16 v[0:15], v[18:21], v[34:37], v[0:15]
	v_add_u32_e32 v18, 8, v158
	v_bitop3_b32 v18, v18, v82, 15 bitop3:0x78
	v_lshl_add_u32 v18, v18, 4, v157
	ds_read_b128 v[18:21], v18
	s_waitcnt vmcnt(25) lgkmcnt(1)
	v_mfma_f32_32x32x16_bf16 v[0:15], v[22:25], v[38:41], v[0:15]
	s_waitcnt vmcnt(20)
	v_mfma_f32_32x32x16_bf16 v[0:15], v[22:25], v[58:61], v[0:15]
	v_add_u32_e32 v22, 10, v158
	v_bitop3_b32 v22, v22, v82, 15 bitop3:0x78
	v_lshl_add_u32 v22, v22, 4, v157
	ds_read_b128 v[22:25], v22
	s_waitcnt lgkmcnt(1)
	v_mfma_f32_32x32x16_bf16 v[0:15], v[18:21], v[42:45], v[0:15]
	v_mfma_f32_32x32x16_bf16 v[0:15], v[18:21], v[46:49], v[0:15]
	v_add_u32_e32 v18, 12, v158
	v_bitop3_b32 v18, v18, v82, 15 bitop3:0x78
	v_lshl_add_u32 v18, v18, 4, v157
	ds_read_b128 v[18:21], v18
	s_waitcnt lgkmcnt(1)
	v_mfma_f32_32x32x16_bf16 v[0:15], v[22:25], v[50:53], v[0:15]
	v_mfma_f32_32x32x16_bf16 v[0:15], v[22:25], v[54:57], v[0:15]
	v_add_u32_e32 v22, 14, v158
	v_bitop3_b32 v22, v22, v82, 15 bitop3:0x78
	v_lshl_add_u32 v22, v22, 4, v157
	ds_read_b128 v[22:25], v22
	s_waitcnt vmcnt(16) lgkmcnt(1)
	v_mfma_f32_32x32x16_bf16 v[0:15], v[18:21], v[74:77], v[0:15]
	v_mfma_f32_32x32x16_bf16 v[0:15], v[18:21], v[62:65], v[0:15]
	v_add_u32_e32 v18, 16, v158
	v_bitop3_b32 v18, v18, v82, 15 bitop3:0x78
	v_lshl_add_u32 v18, v18, 4, v157
	ds_read_b128 v[18:21], v18
	s_waitcnt lgkmcnt(1)
	v_mfma_f32_32x32x16_bf16 v[0:15], v[22:25], v[66:69], v[0:15]
	v_mfma_f32_32x32x16_bf16 v[0:15], v[22:25], v[70:73], v[0:15]
	v_add_u32_e32 v22, 18, v158
	v_bitop3_b32 v22, v22, v82, 15 bitop3:0x78
	v_lshl_add_u32 v22, v22, 4, v157
	ds_read_b128 v[22:25], v22
	s_waitcnt vmcnt(15) lgkmcnt(1)
	v_mfma_f32_32x32x16_bf16 v[0:15], v[18:21], v[84:87], v[0:15]
	s_waitcnt vmcnt(14)
	v_mfma_f32_32x32x16_bf16 v[0:15], v[18:21], v[88:91], v[0:15]
	v_add_u32_e32 v18, 20, v158
	v_bitop3_b32 v18, v18, v82, 15 bitop3:0x78
	v_lshl_add_u32 v18, v18, 4, v157
	ds_read_b128 v[18:21], v18
	s_waitcnt vmcnt(13) lgkmcnt(1)
	v_mfma_f32_32x32x16_bf16 v[0:15], v[22:25], v[92:95], v[0:15]
	s_waitcnt vmcnt(12)
	v_mfma_f32_32x32x16_bf16 v[0:15], v[22:25], v[96:99], v[0:15]
	v_add_u32_e32 v22, 22, v158
	v_bitop3_b32 v22, v22, v82, 15 bitop3:0x78
	v_lshl_add_u32 v22, v22, 4, v157
	ds_read_b128 v[22:25], v22
	s_waitcnt vmcnt(11) lgkmcnt(1)
	v_mfma_f32_32x32x16_bf16 v[0:15], v[18:21], v[100:103], v[0:15]
	s_waitcnt vmcnt(10)
	v_mfma_f32_32x32x16_bf16 v[0:15], v[18:21], v[104:107], v[0:15]
	v_add_u32_e32 v18, 24, v158
	v_bitop3_b32 v18, v18, v82, 15 bitop3:0x78
	v_lshl_add_u32 v18, v18, 4, v157
	ds_read_b128 v[18:21], v18
	s_waitcnt vmcnt(9) lgkmcnt(1)
	v_mfma_f32_32x32x16_bf16 v[0:15], v[22:25], v[108:111], v[0:15]
	s_waitcnt vmcnt(4)
	v_mfma_f32_32x32x16_bf16 v[0:15], v[22:25], v[128:131], v[0:15]
	v_add_u32_e32 v22, 26, v158
	v_bitop3_b32 v22, v22, v82, 15 bitop3:0x78
	v_lshl_add_u32 v22, v22, 4, v157
	ds_read_b128 v[22:25], v22
	s_waitcnt lgkmcnt(1)
	v_mfma_f32_32x32x16_bf16 v[0:15], v[18:21], v[112:115], v[0:15]
	v_mfma_f32_32x32x16_bf16 v[0:15], v[18:21], v[116:119], v[0:15]
	v_add_u32_e32 v18, 28, v158
	v_bitop3_b32 v18, v18, v82, 15 bitop3:0x78
	v_lshl_add_u32 v18, v18, 4, v157
	ds_read_b128 v[18:21], v18
	s_waitcnt lgkmcnt(1)
	v_mfma_f32_32x32x16_bf16 v[0:15], v[22:25], v[120:123], v[0:15]
	v_mfma_f32_32x32x16_bf16 v[0:15], v[22:25], v[124:127], v[0:15]
	v_add_u32_e32 v22, 30, v158
	v_bitop3_b32 v22, v22, v82, 15 bitop3:0x78
	v_lshl_add_u32 v22, v22, 4, v157
	ds_read_b128 v[22:25], v22
	s_waitcnt lgkmcnt(0)
	s_barrier
	s_waitcnt vmcnt(3)
	v_mfma_f32_32x32x16_bf16 v[0:15], v[18:21], v[132:135], v[0:15]
	s_waitcnt vmcnt(2)
	v_mfma_f32_32x32x16_bf16 v[0:15], v[18:21], v[136:139], v[0:15]
	v_lshlrev_b32_e32 v18, 9, v156
	v_lshlrev_b32_e32 v19, 2, v83
	v_add3_u32 v18, s37, v18, v19
	v_add_u32_e32 v19, 0x400, v18
	v_add_u32_e32 v20, 0x800, v18
	v_add_u32_e32 v21, 0xc00, v18
	s_waitcnt vmcnt(1)
	v_mfma_f32_32x32x16_bf16 v[0:15], v[22:25], v[140:143], v[0:15]
	s_waitcnt vmcnt(0)
	v_mfma_f32_32x32x16_bf16 v[0:15], v[22:25], v[144:147], v[0:15]
	s_nop 11
	ds_write2_b32 v18, v0, v1 offset1:32
	ds_write2_b32 v18, v2, v3 offset0:64 offset1:96
	ds_write2_b32 v19, v4, v5 offset1:32
	ds_write2_b32 v19, v6, v7 offset0:64 offset1:96
	ds_write2_b32 v20, v8, v9 offset1:32
	ds_write2_b32 v20, v10, v11 offset0:64 offset1:96
	ds_write2_b32 v21, v12, v13 offset1:32
	ds_write2_b32 v21, v14, v15 offset0:64 offset1:96
	s_waitcnt lgkmcnt(0)
	s_barrier
	s_and_saveexec_b64 s[16:17], s[0:1]
	s_cbranch_execz .LBB0_1045
	ds_read2st64_b32 v[0:1], v81 offset1:16
	ds_read2st64_b32 v[2:3], v81 offset0:32 offset1:48
	ds_read2st64_b32 v[4:5], v81 offset0:64 offset1:80
	ds_read2st64_b32 v[6:7], v81 offset0:96 offset1:112
	v_add_u32_e32 v8, s51, v80
	s_waitcnt lgkmcnt(3)
	v_add_f32_e32 v0, 0, v0
	v_add_f32_e32 v0, v0, v1
	s_waitcnt lgkmcnt(2)
	v_add_f32_e32 v0, v0, v2
	v_add_f32_e32 v0, v0, v3
	s_waitcnt lgkmcnt(1)
	v_add_f32_e32 v0, v0, v4
	v_add_f32_e32 v0, v0, v5
	s_waitcnt lgkmcnt(0)
	v_add_f32_e32 v0, v0, v6
	v_ashrrev_i32_e32 v9, 31, v8
	v_add_f32_e32 v2, v0, v7
	v_lshlrev_b64 v[0:1], 6, v[8:9]
	v_lshl_add_u64 v[0:1], v[16:17], 0, v[0:1]
	global_store_dword v[0:1], v2, off
	s_branch .LBB0_1045
